# stack14 plus attention K/V tile staging by LDS-DMA (global_load_lds_dwordx4 with source-side swizzle into the unchanged LDS image) instead of global_load to VGPR plus ds_write_b128; staging wait moved
# speedup vs baseline: 1.0197x; 1.0197x over previous
; DI int tid_fresh(int wave) { return wave * 64 + lane_fresh(); }
; DI void attn_pass(const Frame& F, CvRide& cv, const bf16_t* __restrict__ Qb, const bf16_t* __restrict__ Kh, const bf16_t* __restrict__ Vh, char* lds, f32x16 (&o)[4], float& l_out, const int wave_s) {
;     const int tid = tid_fresh(wave_s), wid = tid >> 6, lane = tid & 63, r32 = lane & 31, hi = lane >> 5;
;     char* V_lds = lds + OFF_V; char* K_lds = lds + OFF_K;
;     float m_ref = 0.f, l_reg = 0.f; bf16x8 qr[4]; f32x16 negm = f32x16{};
; #pragma unroll
;     for (int d = 0; d < 4; ++d) o[d] = f32x16{};
;     const bf16_t* Qw = Qb + (size_t)(wid * 32 + r32) * 64 + hi * 8;
; #pragma unroll
;     for (int d0 = 0; d0 < 4; ++d0) qr[d0] = *reinterpret_cast<const bf16x8*>(Qw + d0 * 16);
;     const int sr = tid >> 4, sc = (tid & 15) * 8, vst0 = v_st(sr, sc), vst1 = v_st(32 + sr, sc);
;     const int kr = tid >> 3, kcb = (tid & 7) * 16, kst = AT_KSWZ(kr, kcb);
;     const int vb0 = (int)(uintptr_t)V_lds + v_rd_base(lane);
;     struct { bf16x8 vs0, vs1, ks0; } sr_[1];
;     const unsigned gvo = (unsigned)((sr * 128 + sc) * 2), gko = (unsigned)((kr * 64 + (tid & 7) * 8) * 2);
;     ...
;     const unsigned cv_ldo = (unsigned)(((tid >> 4) * 2 * 2048 + (tid & 15) * 4) * 4), cv_sto = (unsigned)((tid >> 3) * 2048 + 8 * (tid & 7));
;     const int cv_lw = OFF_CV + (4 * (tid & 15)) * 68 + 2 * (tid >> 4), cv_lr = OFF_CV + (tid >> 3) * 68 + 8 * (tid & 7);
;     f32x4 cvA = f32x4{}, cvB = f32x4{}; unsigned cvr0 = 0, cvr1 = 0;
;     ...
;     f32x16 pA0, pA1, pB0, pB1; float alA, alB; bf16x8 pa0, pa1, pa2, pa3; constexpr int NT = S / 64;
;     constexpr int SE = 0;
;     {
;         bf16x8 v10 = *reinterpret_cast<const bf16x8*>(&Vh[(size_t)(64 + sr) * 128 + sc]), v11 = *reinterpret_cast<const bf16x8*>(&Vh[(size_t)(96 + sr) * 128 + sc]);
;         bf16x8 k10 = *reinterpret_cast<const bf16x8*>(&Kh[(size_t)(64 + kr) * 64 + (tid & 7) * 8]);
;         AT_SLOAD(SE, 0); asm volatile("s_waitcnt vmcnt(0)" ::: "memory");
;         __syncthreads();
;         AT_SWRITE(0, SE);
;         *(bf16x8*)(V_lds + SHM_V + vst0) = v10; *(bf16x8*)(V_lds + SHM_V + vst1) = v11; *(bf16x8*)(K_lds + SHM_K + kst) = k10;
;         __syncthreads();
;     }
;     qkt(pA0, pA1, K_lds, qr, negm, r32, hi); partialSM(pA0, pA1, m_ref, negm, alA);
;     int s_prev = 0, s_cur = 1, s_next = 2;
.LBB4_691:
	v_lshlrev_b32_e32 v24, 4, v21
	v_lshlrev_b32_e32 v23, 3, v21
	v_and_b32_e32 v24, 0xc0, v24
	v_lshlrev_b32_e32 v21, 1, v21
	v_and_or_b32 v24, v23, 24, v24
	v_and_b32_e32 v21, 32, v21
	v_and_b32_e32 v23, 0x100, v23
	s_cmp_lg_u32 0, -1
	v_or3_b32 v199, v24, v21, v23
	s_cselect_b32 s2, 0, 0
	v_add_u32_e32 v192, s2, v199
	s_movk_i32 s2, 0x44
	v_lshl_or_b32 v209, v16, 14, v18
	v_mul_lo_u32 v16, v20, s2
	v_exp_f32_e32 v216, v0
	v_exp_f32_e32 v218, v1
	v_exp_f32_e32 v179, v2
	v_exp_f32_e32 v217, v3
	v_exp_f32_e32 v177, v4
	v_exp_f32_e32 v215, v5
	v_exp_f32_e32 v176, v6
	v_exp_f32_e32 v178, v7
	v_exp_f32_e32 v173, v8
	v_exp_f32_e32 v175, v9
	v_exp_f32_e32 v171, v10
	v_exp_f32_e32 v174, v11
	v_exp_f32_e32 v169, v12
	v_exp_f32_e32 v172, v13
	v_exp_f32_e32 v168, v14
	v_exp_f32_e32 v170, v15
	v_add_u32_e32 v0, 0, v19
	s_mov_b32 s2, 0x22000
	v_mov_b32_e32 v182, 0
	v_add3_u32 v190, v0, v16, s2
	v_add_u32_e32 v0, 0, v22
	v_mov_b32_e32 v162, v182
	v_mov_b32_e32 v163, v182
	v_mov_b32_e32 v32, v182
	v_mov_b32_e32 v33, v182
	v_mov_b32_e32 v46, v182
	v_mov_b32_e32 v47, v182
	v_lshl_or_b32 v189, v20, 11, v19
	v_add3_u32 v191, v0, v17, s2
	v_mov_b32_e32 v183, v182
	v_mov_b32_e32 v160, v182
	v_mov_b32_e32 v161, v182
	v_mov_b32_e32 v34, v182
	v_mov_b32_e32 v35, v182
	v_mov_b32_e32 v36, v182
	v_mov_b32_e32 v37, v182
	v_mov_b32_e32 v38, v182
	v_mov_b32_e32 v39, v182
	v_mov_b32_e32 v40, v182
	v_mov_b32_e32 v41, v182
	v_mov_b32_e32 v42, v182
	v_mov_b32_e32 v43, v182
	v_mov_b32_e32 v44, v182
	v_mov_b32_e32 v45, v182
	v_mov_b64_e32 v[62:63], v[46:47]
	v_mov_b64_e32 v[16:17], v[32:33]
	v_mov_b64_e32 v[0:1], v[32:33]
	v_mov_b64_e32 v[166:167], v[162:163]
	s_mov_b32 s36, -1
	s_mul_i32 s59, s33, 6
	s_mov_b32 s64, 2
	s_mov_b64 s[12:13], 0
	s_mov_b32 s62, 0xc3e00000
	v_mov_b32_e32 v211, 0x43e00000
	s_mov_b64 s[28:29], s[16:17]
	s_mov_b64 s[30:31], s[18:19]
	s_mov_b32 s58, 0
	s_mov_b32 s26, 0
	s_mov_b64 s[10:11], 0
	s_mov_b64 s[8:9], 0
	v_mov_b64_e32 v[60:61], v[44:45]
	v_mov_b64_e32 v[58:59], v[42:43]
	v_mov_b64_e32 v[56:57], v[40:41]
	v_mov_b64_e32 v[54:55], v[38:39]
	v_mov_b64_e32 v[52:53], v[36:37]
	v_mov_b64_e32 v[50:51], v[34:35]
	v_mov_b64_e32 v[48:49], v[32:33]
	v_mov_b64_e32 v[18:19], v[34:35]
	v_mov_b64_e32 v[20:21], v[36:37]
	v_mov_b64_e32 v[22:23], v[38:39]
	v_mov_b64_e32 v[24:25], v[40:41]
	v_mov_b64_e32 v[26:27], v[42:43]
	v_mov_b64_e32 v[28:29], v[44:45]
	v_mov_b64_e32 v[30:31], v[46:47]
	v_mov_b64_e32 v[2:3], v[34:35]
	v_mov_b64_e32 v[4:5], v[36:37]
	v_mov_b64_e32 v[6:7], v[38:39]
	v_mov_b64_e32 v[8:9], v[40:41]
	v_mov_b64_e32 v[10:11], v[42:43]
	v_mov_b64_e32 v[12:13], v[44:45]
	v_mov_b64_e32 v[14:15], v[46:47]
	v_mov_b64_e32 v[164:165], v[160:161]
	s_mov_b32 s34, 0
	s_mov_b32 s65, 1
	v_mov_b64_e32 v[184:185], v[182:183]
	v_mov_b32_e32 v81, v80
	v_mov_b32_e32 v82, v80
	v_mov_b32_e32 v83, v80
	v_mov_b32_e32 v84, v80
	v_mov_b32_e32 v85, v80
	v_mov_b32_e32 v86, v80
	v_mov_b32_e32 v87, v80
	v_mov_b32_e32 v88, v80
	v_mov_b32_e32 v89, v80
	v_mov_b32_e32 v90, v80
	v_mov_b32_e32 v91, v80
	v_mov_b32_e32 v92, v80
	v_mov_b32_e32 v93, v80
	v_mov_b32_e32 v94, v80
	v_mov_b32_e32 v95, v80
	v_mov_b32_e32 v255, 0x3f600000
	s_mov_b32 s93, 0x3b000000
	v_mbcnt_lo_u32_b32 v253, -1, 0
	v_mbcnt_hi_u32_b32 v253, -1, v253
	v_lshrrev_b32_e32 v253, 5, v253
	v_mul_u32_u24_e32 v253, 0x700, v253
	v_add_u32_e32 v253, v253, v192
	v_mbcnt_lo_u32_b32 v249, -1, 0
	v_mbcnt_hi_u32_b32 v249, -1, v249
	v_bfe_u32 v250, v249, 4, 1
	v_lshlrev_b32_e32 v250, 11, v250
	v_bfe_u32 v251, v249, 2, 2
	v_lshl_add_u32 v250, v251, 8, v250
	v_lshrrev_b32_e32 v251, 5, v249
	v_lshl_add_u32 v250, v251, 6, v250
	v_and_b32_e32 v251, 3, v249
	v_lshl_add_u32 v250, v251, 4, v250
	s_and_b32 s95, s69, 1
	s_lshr_b32 s94, s69, 1
	s_lshl_b32 s94, s94, 12
	s_lshl_b32 s96, s95, 10
	s_add_i32 s94, s94, s96
	v_lshrrev_b32_e32 v251, 4, v249
	v_lshl_add_u32 v251, s95, 2, v251
	v_and_b32_e32 v254, 7, v249
	v_xor_b32_e32 v251, v251, v254
	v_lshlrev_b32_e32 v251, 4, v251
	v_lshrrev_b32_e32 v254, 3, v249
	v_lshl_add_u32 v251, v254, 7, v251
	s_lshl_b32 s96, s69, 10
	v_add_u32_e32 v251, s96, v251
	v_add_u32_e32 v249, s94, v250
	v_add_u32_e32 v250, 0x80, v249
	s_lshl_b32 s94, s69, 11
	s_add_i32 s95, s96, 0xc000
	s_nop 0

; DI void finishSM(f32x16& p0, f32x16& p1, float alpha, float& l_reg, bf16x8& pa0, bf16x8& pa1, bf16x8& pa2, bf16x8& pa3) {
; #pragma unroll
;     for (int r = 0; r < 16; ++r) p1[r] = __builtin_amdgcn_exp2f(p1[r]);
;     float ps = 0;
; #pragma unroll
;     for (int r = 0; r < 16; ++r) ps += p0[r];
; #pragma unroll
;     for (int r = 0; r < 16; ++r) ps += p1[r];
;     { auto rr = __builtin_amdgcn_permlane32_swap(__float_as_uint(ps), __float_as_uint(ps), false, false); ps = __uint_as_float(rr[0]) + __uint_as_float(rr[1]); }
;     l_reg = l_reg * alpha + ps;
;     ...
;     AT_PK4(p0, 0, pa0); AT_PK4(p0, 8, pa1); AT_PK4(p1, 0, pa2); AT_PK4(p1, 8, pa3);
;     ...
; }
; DI void qkt(f32x16& p0, f32x16& p1, const char* Ks, const bf16x8* qr, const f32x16& negm, int r32, int hi) {
; #pragma unroll
;     for (int d0 = 0; d0 < 4; ++d0) { const int cb = (d0 * 16 + hi * 8) * 2;
;         const bf16x8 b0 = *reinterpret_cast<const bf16x8*>(Ks + AT_KSWZ(r32, cb));
;         const bf16x8 b1 = *reinterpret_cast<const bf16x8*>(Ks + AT_KSWZ(32 + r32, cb));
;         p0 = __builtin_amdgcn_mfma_f32_32x32x16_bf16(b0, qr[d0], d0 == 0 ? negm : p0, 0, 0, 0);
;         p1 = __builtin_amdgcn_mfma_f32_32x32x16_bf16(b1, qr[d0], d0 == 0 ? negm : p1, 0, 0, 0); }
; }
.LBB4_702:
	s_lshl_b32 s26, s66, 13
	s_add_i32 s26, s26, 0
	v_add_u32_e32 v72, s26, v205
	v_add_u32_e32 v112, s26, v206
	v_add_u32_e32 v180, s26, v207
	s_waitcnt lgkmcnt(1)
	v_mfma_f32_32x32x16_bf16 v[128:143], v[64:67], v[156:159], v[80:95]
	ds_read_b128 v[64:67], v72 offset:49152
	ds_read_b128 v[72:75], v72 offset:53248
	ds_read_b128 v[76:79], v112 offset:49152
	ds_read_b128 v[220:223], v112 offset:53248
	v_exp_f32_e32 v186, v97
	v_exp_f32_e32 v213, v98
	v_exp_f32_e32 v214, v99
	v_exp_f32_e32 v219, v100
	v_exp_f32_e32 v228, v101
	s_waitcnt lgkmcnt(4)
	v_mfma_f32_32x32x16_bf16 v[112:127], v[68:71], v[156:159], v[80:95]
	ds_read_b128 v[68:71], v180 offset:49152
	ds_read_b128 v[224:227], v180 offset:53248
	v_exp_f32_e32 v180, v96
	v_cvt_pk_bf16_f32 v96, v216, v218
	v_cvt_pk_bf16_f32 v97, v179, v217
	v_cvt_pk_bf16_f32 v98, v177, v215
	v_cvt_pk_bf16_f32 v99, v176, v178
	s_waitcnt lgkmcnt(4)
	v_mfma_f32_32x32x16_bf16 v[112:127], v[72:75], v[152:155], v[112:127]
	v_add_f32_e32 v75, 0, v216
	v_add_f32_e32 v75, v218, v75
	v_add_f32_e32 v75, v179, v75
	v_add_f32_e32 v75, v217, v75
	v_add_f32_e32 v75, v177, v75
	v_add_f32_e32 v75, v215, v75
	v_add_f32_e32 v75, v176, v75
	v_mfma_f32_32x32x16_bf16 v[128:143], v[64:67], v[152:155], v[128:143]
	v_add_f32_e32 v75, v178, v75
	v_add_f32_e32 v75, v173, v75
	v_add_f32_e32 v75, v175, v75
	v_add_f32_e32 v75, v171, v75
	v_add_f32_e32 v75, v174, v75
	v_add_f32_e32 v75, v169, v75
	v_add_f32_e32 v75, v172, v75
	s_waitcnt lgkmcnt(3)
	v_mfma_f32_32x32x16_bf16 v[128:143], v[76:79], v[148:151], v[128:143]
	v_add_f32_e32 v75, v168, v75
	v_add_f32_e32 v75, v170, v75
	v_add_f32_e32 v75, v180, v75
	v_add_f32_e32 v75, v186, v75
	v_exp_f32_e32 v64, v102
	v_exp_f32_e32 v65, v103
	v_exp_f32_e32 v66, v104
	s_waitcnt lgkmcnt(2)
	v_mfma_f32_32x32x16_bf16 v[112:127], v[220:223], v[148:151], v[112:127]
	v_exp_f32_e32 v67, v105
	v_exp_f32_e32 v105, v106
	v_exp_f32_e32 v106, v107
	v_exp_f32_e32 v107, v108
	v_exp_f32_e32 v72, v109
	v_exp_f32_e32 v73, v110
	v_exp_f32_e32 v74, v111
	s_waitcnt lgkmcnt(1)
	v_mfma_f32_32x32x16_bf16 v[128:143], v[68:71], v[144:147], v[128:143]
	v_add_f32_e32 v68, v213, v75
	v_add_f32_e32 v68, v214, v68
	v_add_f32_e32 v68, v219, v68
	v_add_f32_e32 v68, v228, v68
	v_add_f32_e32 v68, v64, v68
	v_add_f32_e32 v68, v65, v68
	v_add_f32_e32 v68, v66, v68
	v_add_f32_e32 v68, v67, v68
	s_waitcnt lgkmcnt(0)
	v_mfma_f32_32x32x16_bf16 v[112:127], v[224:227], v[144:147], v[112:127]
	v_add_f32_e32 v68, v105, v68
	v_add_f32_e32 v68, v106, v68
	v_add_f32_e32 v68, v107, v68
	v_add_f32_e32 v68, v72, v68
	v_add_f32_e32 v68, v73, v68
	v_add_f32_e32 v183, v74, v68
	v_cvt_pk_bf16_f32 v108, v173, v175
	v_cvt_pk_bf16_f32 v109, v171, v174
	v_cvt_pk_bf16_f32 v110, v169, v172
	v_cvt_pk_bf16_f32 v111, v168, v170
	v_cvt_pk_bf16_f32 v100, v180, v186
	v_cvt_pk_bf16_f32 v101, v213, v214
	v_cvt_pk_bf16_f32 v102, v219, v228
	v_cvt_pk_bf16_f32 v103, v64, v65
	v_cvt_pk_bf16_f32 v104, v66, v67
	v_cvt_pk_bf16_f32 v105, v105, v106
	v_cvt_pk_bf16_f32 v106, v107, v72
	v_cvt_pk_bf16_f32 v107, v73, v74
	s_add_u32 s74, s46, s28
	s_addc_u32 s75, s47, s29
	s_add_u32 s78, s74, 0x23808000
	s_addc_u32 s79, s75, 0
	s_add_u32 s80, s74, 0x2380a000
	s_addc_u32 s81, s75, 0
	s_add_u32 s76, s46, s30
	s_addc_u32 s77, s47, s31
	s_add_u32 s82, s76, 0x21804000
	s_addc_u32 s83, s77, 0
	s_lshl_b32 s92, s64, 14
	s_add_i32 s92, s92, s94
	s_mov_b32 m0, s92
	s_lshl_b32 s96, s64, 13
	global_load_lds_dwordx4 v249, s[78:79]
	s_addk_i32 s92, 0x400
	s_mov_b32 m0, s92
	s_add_i32 s96, s96, s95
	global_load_lds_dwordx4 v250, s[78:79]
	s_nop 0
	s_mov_b32 m0, s96
	s_nop 0
	global_load_lds_dwordx4 v251, s[82:83]
	s_andn2_b64 vcc, exec, s[2:3]
	s_cbranch_vccnz .LBB4_704
	s_mov_b64 s[2:3], s[8:9]
	global_store_dwordx2 v189, v[184:185], s[2:3] nt

; #define AT_SBAR() __builtin_amdgcn_sched_barrier(0)
; template <int OFF> DI s16x4 tr_read(int vb) { s16x4 r; asm volatile("ds_read_b64_tr_b16 %0, %1 offset:%2" : "=&v"(r) : "v"(vb), "i"(OFF) : "memory"); return r; }
; template <int D0> DI void pv_one(f32x16& od, int vb, bf16x8 pa0, bf16x8 pa1, bf16x8 pa2, bf16x8 pa3) {
;     const s16x4 l0 = tr_read<v_rd_off(D0, 0, 0)>(vb), h0 = tr_read<v_rd_off(D0, 0, 1)>(vb), l1 = tr_read<v_rd_off(D0, 1, 0)>(vb), h1 = tr_read<v_rd_off(D0, 1, 1)>(vb);
;     const s16x4 l2 = tr_read<v_rd_off(D0, 2, 0)>(vb), h2 = tr_read<v_rd_off(D0, 2, 1)>(vb), l3 = tr_read<v_rd_off(D0, 3, 0)>(vb), h3 = tr_read<v_rd_off(D0, 3, 1)>(vb);
;     asm volatile("s_waitcnt lgkmcnt(0)" ::: "memory"); AT_SBAR();
;     ...
;     od = __builtin_amdgcn_mfma_f32_32x32x16_bf16(AT_PK(l0, h0), pa0, od, 0, 0, 0);
;     od = __builtin_amdgcn_mfma_f32_32x32x16_bf16(AT_PK(l1, h1), pa1, od, 0, 0, 0);
;     od = __builtin_amdgcn_mfma_f32_32x32x16_bf16(AT_PK(l2, h2), pa2, od, 0, 0, 0);
;     od = __builtin_amdgcn_mfma_f32_32x32x16_bf16(AT_PK(l3, h3), pa3, od, 0, 0, 0);
; DI void attn_pass(const Frame& F, CvRide& cv, const bf16_t* __restrict__ Qb, const bf16_t* __restrict__ Kh, const bf16_t* __restrict__ Vh, char* lds, f32x16 (&o)[4], float& l_out, const int wave_s) {
;     ...
;     const unsigned cv_ldo = (unsigned)(((tid >> 4) * 2 * 2048 + (tid & 15) * 4) * 4), cv_sto = (unsigned)((tid >> 3) * 2048 + 8 * (tid & 7));
;     const int cv_lw = OFF_CV + (4 * (tid & 15)) * 68 + 2 * (tid >> 4), cv_lr = OFF_CV + (tid >> 3) * 68 + 8 * (tid & 7);
;     f32x4 cvA = f32x4{}, cvB = f32x4{}; unsigned cvr0 = 0, cvr1 = 0;
.LBB4_706:
	ds_read_b64_tr_b16 v[214:215], v186 offset:0x600
	ds_read_b64_tr_b16 v[216:217], v186 offset:0x700
	ds_read_b64_tr_b16 v[218:219], v186 offset:0x1600
	ds_read_b64_tr_b16 v[220:221], v186 offset:0x1700
	ds_read_b64_tr_b16 v[222:223], v186 offset:0x2600
	ds_read_b64_tr_b16 v[224:225], v186 offset:0x2700
	ds_read_b64_tr_b16 v[226:227], v186 offset:0x3600
	ds_read_b64_tr_b16 v[228:229], v186 offset:0x3700
	s_waitcnt lgkmcnt(0)
	v_mfma_f32_32x32x16_bf16 v[0:15], v[214:217], v[96:99], v[0:15]
	s_lshl_b32 s2, s64, 14
	s_lshl_b32 s3, s64, 13
	s_sub_i32 s78, s2, s3
	s_waitcnt vmcnt(3)
	v_mfma_f32_32x32x16_bf16 v[0:15], v[218:221], v[108:111], v[0:15]
	s_andn2_b64 s[2:3], exec, s[34:35]
	s_andn2_b64 vcc, exec, s[34:35]
	v_mfma_f32_32x32x16_bf16 v[0:15], v[222:225], v[100:103], v[0:15]
	v_mfma_f32_32x32x16_bf16 v[0:15], v[226:229], v[104:107], v[0:15]
	s_cbranch_vccnz .LBB4_711
	v_med3_f32 v97, v160, -v255, v255
	v_med3_f32 v98, v164, -v255, v255
	v_cvt_scalef32_pk_fp8_f32 v99, v97, v98, s93
	v_med3_f32 v97, v161, -v255, v255
	v_med3_f32 v98, v165, -v255, v255
	v_cvt_scalef32_pk_fp8_f32 v100, v97, v98, s93
	v_med3_f32 v97, v162, -v255, v255
	v_med3_f32 v98, v166, -v255, v255
	s_bitcmp1_b32 s58, 0
	v_cvt_scalef32_pk_fp8_f32 v101, v97, v98, s93
	s_cselect_b32 s8, 0x1100, 0
	v_med3_f32 v97, v163, -v255, v255
	v_med3_f32 v98, v167, -v255, v255
	v_cmp_eq_u32_e32 vcc, 0, v181
	v_add_u32_e32 v96, s8, v191
	v_cvt_scalef32_pk_fp8_f32 v102, v97, v98, s93
	s_and_b64 vcc, exec, vcc
	s_and_b32 s34, s58, 31
	ds_write_b16 v96, v99
	ds_write_b16 v96, v100 offset:68
	ds_write_b16 v96, v101 offset:136
	ds_write_b16 v96, v102 offset:204
	s_cbranch_vccnz .LBB4_735
	s_lshl_b32 s8, s34, 7
	s_lshl_b32 s9, s58, 6
	s_and_b32 s8, s8, 0xf00
	s_and_b32 s9, s9, 64
	s_or_b32 s26, s8, s9
	s_cbranch_execnz .LBB4_710

.LBB4_713:
	s_and_b64 vcc, exec, s[2:3]
	s_waitcnt vmcnt(0) lgkmcnt(0)
	s_barrier
	v_add_u32_e32 v100, s78, v204
	ds_read_b128 v[96:99], v100 offset:49152
	ds_read_b128 v[168:171], v100 offset:53248
	s_cbranch_vccnz .LBB4_715
	s_andn2_b32 s26, 1, s58
	s_mulk_i32 s26, 0x1100
	v_add_u32_e32 v252, s26, v190
	ds_read2_b32 v[184:185], v252 offset1:1

; DI void finishSM(f32x16& p0, f32x16& p1, float alpha, float& l_reg, bf16x8& pa0, bf16x8& pa1, bf16x8& pa2, bf16x8& pa3) {
; #pragma unroll
;     for (int r = 0; r < 16; ++r) p1[r] = __builtin_amdgcn_exp2f(p1[r]);
;     float ps = 0;
; #pragma unroll
;     for (int r = 0; r < 16; ++r) ps += p0[r];
; #pragma unroll
;     for (int r = 0; r < 16; ++r) ps += p1[r];
;     { auto rr = __builtin_amdgcn_permlane32_swap(__float_as_uint(ps), __float_as_uint(ps), false, false); ps = __uint_as_float(rr[0]) + __uint_as_float(rr[1]); }
;     l_reg = l_reg * alpha + ps;
;     ...
;     AT_PK4(p0, 0, pa0); AT_PK4(p0, 8, pa1); AT_PK4(p1, 0, pa2); AT_PK4(p1, 8, pa3);
;     ...
; }
; DI void qkt(f32x16& p0, f32x16& p1, const char* Ks, const bf16x8* qr, const f32x16& negm, int r32, int hi) {
; #pragma unroll
;     for (int d0 = 0; d0 < 4; ++d0) { const int cb = (d0 * 16 + hi * 8) * 2;
;         const bf16x8 b0 = *reinterpret_cast<const bf16x8*>(Ks + AT_KSWZ(r32, cb));
;         const bf16x8 b1 = *reinterpret_cast<const bf16x8*>(Ks + AT_KSWZ(32 + r32, cb));
;         p0 = __builtin_amdgcn_mfma_f32_32x32x16_bf16(b0, qr[d0], d0 == 0 ? negm : p0, 0, 0, 0);
;         p1 = __builtin_amdgcn_mfma_f32_32x32x16_bf16(b1, qr[d0], d0 == 0 ? negm : p1, 0, 0, 0); }
; }
.LBB4_723:
	v_exp_f32_e32 v186, v128
	v_exp_f32_e32 v230, v129
	v_exp_f32_e32 v231, v130
	v_exp_f32_e32 v232, v131
	v_exp_f32_e32 v233, v132
	v_exp_f32_e32 v234, v133
	v_exp_f32_e32 v235, v134
	v_exp_f32_e32 v236, v135
	v_exp_f32_e32 v237, v136
	v_exp_f32_e32 v238, v137
	v_exp_f32_e32 v239, v138
	v_exp_f32_e32 v240, v139
	v_exp_f32_e32 v241, v140
	v_exp_f32_e32 v242, v141
	v_exp_f32_e32 v243, v142
	v_exp_f32_e32 v244, v143
	v_add_u32_e32 v101, s78, v205
	v_add_u32_e32 v102, s78, v206
	v_add_u32_e32 v103, s78, v207
	ds_read_b128 v[172:175], v101 offset:49152
	ds_read_b128 v[176:179], v101 offset:53248
	ds_read_b128 v[214:217], v102 offset:49152
	ds_read_b128 v[218:221], v102 offset:53248
	ds_read_b128 v[222:225], v103 offset:49152
	ds_read_b128 v[226:229], v103 offset:53248
	v_exp_f32_e32 v112, v112
	v_exp_f32_e32 v113, v113
	v_exp_f32_e32 v114, v114
	s_waitcnt lgkmcnt(7)
	v_mfma_f32_32x32x16_bf16 v[128:143], v[96:99], v[156:159], v[80:95]
	v_exp_f32_e32 v115, v115
	v_exp_f32_e32 v116, v116
	v_exp_f32_e32 v117, v117
	v_exp_f32_e32 v118, v118
	v_exp_f32_e32 v119, v119
	s_waitcnt lgkmcnt(6)
	v_mfma_f32_32x32x16_bf16 v[96:111], v[168:171], v[156:159], v[80:95]
	v_exp_f32_e32 v168, v120
	v_add_f32_e32 v120, 0, v186
	v_add_f32_e32 v120, v230, v120
	v_add_f32_e32 v120, v231, v120
	v_add_f32_e32 v120, v232, v120
	v_add_f32_e32 v120, v233, v120
	v_add_f32_e32 v120, v234, v120
	v_add_f32_e32 v120, v235, v120
	v_add_f32_e32 v120, v236, v120
	v_add_f32_e32 v120, v237, v120
	v_add_f32_e32 v120, v238, v120
	s_waitcnt lgkmcnt(5)
	v_mfma_f32_32x32x16_bf16 v[128:143], v[172:175], v[152:155], v[128:143]
	v_add_f32_e32 v120, v239, v120
	v_add_f32_e32 v120, v240, v120
	v_add_f32_e32 v120, v241, v120
	v_add_f32_e32 v120, v242, v120
	v_add_f32_e32 v120, v243, v120
	v_add_f32_e32 v120, v244, v120
	v_add_f32_e32 v120, v112, v120
	s_waitcnt lgkmcnt(4)
	v_mfma_f32_32x32x16_bf16 v[96:111], v[176:179], v[152:155], v[96:111]
	v_add_f32_e32 v120, v113, v120
	v_add_f32_e32 v120, v114, v120
	v_add_f32_e32 v120, v115, v120
	v_add_f32_e32 v120, v116, v120
	v_exp_f32_e32 v169, v121
	v_add_f32_e32 v120, v117, v120
	v_exp_f32_e32 v170, v122
	s_waitcnt lgkmcnt(3)
	v_mfma_f32_32x32x16_bf16 v[128:143], v[214:217], v[148:151], v[128:143]
	v_add_f32_e32 v120, v118, v120
	v_exp_f32_e32 v171, v123
	v_add_f32_e32 v120, v119, v120
	v_exp_f32_e32 v172, v124
	v_add_f32_e32 v120, v168, v120
	v_exp_f32_e32 v173, v125
	v_add_f32_e32 v120, v169, v120
	s_waitcnt lgkmcnt(2)
	v_mfma_f32_32x32x16_bf16 v[96:111], v[218:221], v[148:151], v[96:111]
	v_exp_f32_e32 v174, v126
	v_add_f32_e32 v120, v170, v120
	v_exp_f32_e32 v175, v127
	v_add_f32_e32 v120, v171, v120
	v_add_f32_e32 v120, v172, v120
	v_add_f32_e32 v120, v173, v120
	v_add_f32_e32 v120, v174, v120
	s_waitcnt lgkmcnt(1)
	v_mfma_f32_32x32x16_bf16 v[128:143], v[222:225], v[144:147], v[128:143]
	v_add_f32_e32 v213, v175, v120
	v_cvt_pk_bf16_f32 v120, v186, v230
	v_cvt_pk_bf16_f32 v121, v231, v232
	v_cvt_pk_bf16_f32 v122, v233, v234
	v_cvt_pk_bf16_f32 v123, v235, v236
	v_cvt_pk_bf16_f32 v124, v237, v238
	s_waitcnt lgkmcnt(0)
	v_mfma_f32_32x32x16_bf16 v[96:111], v[226:229], v[144:147], v[96:111]
	v_cvt_pk_bf16_f32 v125, v239, v240
	v_cvt_pk_bf16_f32 v126, v241, v242
	v_cvt_pk_bf16_f32 v127, v243, v244
	v_cvt_pk_bf16_f32 v112, v112, v113
	v_cvt_pk_bf16_f32 v113, v114, v115
	v_cvt_pk_bf16_f32 v114, v116, v117
	v_cvt_pk_bf16_f32 v115, v118, v119
	v_cvt_pk_bf16_f32 v116, v168, v169
	v_cvt_pk_bf16_f32 v117, v170, v171
	v_cvt_pk_bf16_f32 v118, v172, v173
	v_cvt_pk_bf16_f32 v119, v174, v175
	s_add_u32 s78, s74, 0x2380c000
	s_addc_u32 s79, s75, 0
	s_add_u32 s74, s74, 0x2380e000
	s_addc_u32 s75, s75, 0
	s_add_u32 s76, s76, 0x21806000
	s_addc_u32 s77, s77, 0
	s_lshl_b32 s92, s65, 14
	s_add_i32 s92, s92, s94
	s_mov_b32 m0, s92
	s_lshl_b32 s96, s65, 13
	global_load_lds_dwordx4 v249, s[78:79]
	s_addk_i32 s92, 0x400
	s_mov_b32 m0, s92
	s_add_i32 s96, s96, s95
	global_load_lds_dwordx4 v250, s[78:79]
	s_nop 0
	s_mov_b32 m0, s96
	s_nop 0
	global_load_lds_dwordx4 v251, s[76:77]
	s_nop 0
	s_and_b64 vcc, exec, s[2:3]
	s_cbranch_vccnz .LBB4_725
	s_mov_b64 s[2:3], s[8:9]
	global_store_dwordx2 v189, v[184:185], s[2:3] nt

; #define AT_SBAR() __builtin_amdgcn_sched_barrier(0)
; template <int OFF> DI s16x4 tr_read(int vb) { s16x4 r; asm volatile("ds_read_b64_tr_b16 %0, %1 offset:%2" : "=&v"(r) : "v"(vb), "i"(OFF) : "memory"); return r; }
; template <int D0> DI void pv_one(f32x16& od, int vb, bf16x8 pa0, bf16x8 pa1, bf16x8 pa2, bf16x8 pa3) {
;     const s16x4 l0 = tr_read<v_rd_off(D0, 0, 0)>(vb), h0 = tr_read<v_rd_off(D0, 0, 1)>(vb), l1 = tr_read<v_rd_off(D0, 1, 0)>(vb), h1 = tr_read<v_rd_off(D0, 1, 1)>(vb);
;     const s16x4 l2 = tr_read<v_rd_off(D0, 2, 0)>(vb), h2 = tr_read<v_rd_off(D0, 2, 1)>(vb), l3 = tr_read<v_rd_off(D0, 3, 0)>(vb), h3 = tr_read<v_rd_off(D0, 3, 1)>(vb);
;     asm volatile("s_waitcnt lgkmcnt(0)" ::: "memory"); AT_SBAR();
;     ...
;     od = __builtin_amdgcn_mfma_f32_32x32x16_bf16(AT_PK(l0, h0), pa0, od, 0, 0, 0);
;     od = __builtin_amdgcn_mfma_f32_32x32x16_bf16(AT_PK(l1, h1), pa1, od, 0, 0, 0);
;     od = __builtin_amdgcn_mfma_f32_32x32x16_bf16(AT_PK(l2, h2), pa2, od, 0, 0, 0);
;     od = __builtin_amdgcn_mfma_f32_32x32x16_bf16(AT_PK(l3, h3), pa3, od, 0, 0, 0);
; DI void attn_pass(const Frame& F, CvRide& cv, const bf16_t* __restrict__ Qb, const bf16_t* __restrict__ Kh, const bf16_t* __restrict__ Vh, char* lds, f32x16 (&o)[4], float& l_out, const int wave_s) {
;     ...
;     const unsigned cv_ldo = (unsigned)(((tid >> 4) * 2 * 2048 + (tid & 15) * 4) * 4), cv_sto = (unsigned)((tid >> 3) * 2048 + 8 * (tid & 7));
;     const int cv_lw = OFF_CV + (4 * (tid & 15)) * 68 + 2 * (tid >> 4), cv_lr = OFF_CV + (tid >> 3) * 68 + 8 * (tid & 7);
;     f32x4 cvA = f32x4{}, cvB = f32x4{}; unsigned cvr0 = 0, cvr1 = 0;
.LBB4_726:
	ds_read_b64_tr_b16 v[216:217], v215 offset:0x600
	ds_read_b64_tr_b16 v[218:219], v215 offset:0x700
	ds_read_b64_tr_b16 v[220:221], v215 offset:0x1600
	ds_read_b64_tr_b16 v[222:223], v215 offset:0x1700
	ds_read_b64_tr_b16 v[224:225], v215 offset:0x2600
	ds_read_b64_tr_b16 v[226:227], v215 offset:0x2700
	ds_read_b64_tr_b16 v[228:229], v215 offset:0x3600
	ds_read_b64_tr_b16 v[230:231], v215 offset:0x3700
	s_waitcnt lgkmcnt(0)
	v_mfma_f32_32x32x16_bf16 v[0:15], v[216:219], v[120:123], v[0:15]
	s_add_i32 s2, s67, 0
	s_waitcnt vmcnt(3)
	s_mov_b32 s26, 0
	s_andn2_b64 vcc, exec, s[34:35]
	v_mfma_f32_32x32x16_bf16 v[0:15], v[220:223], v[124:127], v[0:15]
	v_mfma_f32_32x32x16_bf16 v[0:15], v[224:227], v[112:115], v[0:15]
	s_andn2_b64 s[2:3], exec, s[34:35]
	v_mfma_f32_32x32x16_bf16 v[0:15], v[228:231], v[116:119], v[0:15]
	s_cbranch_vccnz .LBB4_731
	v_med3_f32 v113, v160, -v255, v255
	v_med3_f32 v114, v164, -v255, v255
	v_cvt_scalef32_pk_fp8_f32 v115, v113, v114, s93
	v_med3_f32 v113, v161, -v255, v255
	v_med3_f32 v114, v165, -v255, v255
	v_cvt_scalef32_pk_fp8_f32 v116, v113, v114, s93
	v_med3_f32 v113, v162, -v255, v255
	v_med3_f32 v114, v166, -v255, v255
	s_bitcmp1_b32 s58, 0
	v_cvt_scalef32_pk_fp8_f32 v117, v113, v114, s93
	s_cselect_b32 s8, 0x1100, 0
	v_med3_f32 v113, v163, -v255, v255
	v_med3_f32 v114, v167, -v255, v255
	v_cmp_eq_u32_e32 vcc, 0, v181
	v_add_u32_e32 v112, s8, v191
	v_cvt_scalef32_pk_fp8_f32 v118, v113, v114, s93
	s_and_b64 vcc, exec, vcc
	s_and_b32 s37, s58, 31
	ds_write_b16 v112, v115
	ds_write_b16 v112, v116 offset:68
	ds_write_b16 v112, v117 offset:136
	ds_write_b16 v112, v118 offset:204
	s_cbranch_vccnz .LBB4_736
	s_lshl_b32 s8, s37, 7
	s_lshl_b32 s9, s58, 6
	s_and_b32 s8, s8, 0xf00
	s_and_b32 s9, s9, 64
	s_or_b32 s26, s8, s9
	s_cbranch_execnz .LBB4_730

; DI void pv_all_sm(f32x16* o, int vb, bf16x8 pa0, bf16x8 pa1, bf16x8 pa2, bf16x8 pa3, f32x16& p0, f32x16& p1, float& m_ref, f32x16& negm, float& alpha) {
;     ...
; #pragma unroll
;     for (int r = 0; r < 16; ++r) p0[r] = __builtin_amdgcn_exp2f(p0[r]);
; DI void attn_pass(const Frame& F, CvRide& cv, const bf16_t* __restrict__ Qb, const bf16_t* __restrict__ Kh, const bf16_t* __restrict__ Vh, char* lds, f32x16 (&o)[4], float& l_out, const int wave_s) {
;     ...
;     for (int j = 1; j + 2 < NT; j += 2) {
;         AT_STEP(pB0, pB1, pA0, pA1, alB, alA, j, true);
;         AT_STEP(pA0, pA1, pB0, pB1, alA, alB, j + 1, true);
;     }
.LBB4_733:
	s_add_u32 s30, s30, 0x4000
	v_exp_f32_e32 v216, v128
	v_exp_f32_e32 v218, v129
	v_exp_f32_e32 v179, v130
	v_exp_f32_e32 v217, v131
	v_exp_f32_e32 v177, v132
	v_exp_f32_e32 v215, v133
	v_exp_f32_e32 v176, v134
	v_exp_f32_e32 v178, v135
	v_exp_f32_e32 v173, v136
	v_exp_f32_e32 v175, v137
	v_exp_f32_e32 v171, v138
	v_exp_f32_e32 v174, v139
	v_exp_f32_e32 v169, v140
	v_exp_f32_e32 v172, v141
	v_exp_f32_e32 v168, v142
	v_exp_f32_e32 v170, v143
	s_addc_u32 s31, s31, 0
	s_add_u32 s28, s28, 0x8000
	v_fma_f32 v112, v210, v182, v183
	s_addc_u32 s29, s29, 0
	s_add_i32 s15, s15, 2
	v_fma_f32 v182, v112, v180, v213
	s_cmp_gt_u32 s15, 61
	s_waitcnt vmcnt(0) lgkmcnt(0)
	s_barrier
	s_cbranch_scc1 .LBB4_739
	s_mov_b32 s34, s64
	s_mov_b32 s64, s66
	v_mov_b32_e32 v210, v186
	s_branch .LBB4_692

; DI int tid_fresh(int wave) { return wave * 64 + lane_fresh(); }
; DI void attn_pass(const Frame& F, CvRide& cv, const bf16_t* __restrict__ Qb, const bf16_t* __restrict__ Kh, const bf16_t* __restrict__ Vh, char* lds, f32x16 (&o)[4], float& l_out, const int wave_s) {
;     const int tid = tid_fresh(wave_s), wid = tid >> 6, lane = tid & 63, r32 = lane & 31, hi = lane >> 5;
;     char* V_lds = lds + OFF_V; char* K_lds = lds + OFF_K;
;     float m_ref = 0.f, l_reg = 0.f; bf16x8 qr[4]; f32x16 negm = f32x16{};
; #pragma unroll
;     for (int d = 0; d < 4; ++d) o[d] = f32x16{};
;     const bf16_t* Qw = Qb + (size_t)(wid * 32 + r32) * 64 + hi * 8;
; #pragma unroll
;     for (int d0 = 0; d0 < 4; ++d0) qr[d0] = *reinterpret_cast<const bf16x8*>(Qw + d0 * 16);
;     const int sr = tid >> 4, sc = (tid & 15) * 8, vst0 = v_st(sr, sc), vst1 = v_st(32 + sr, sc);
;     const int kr = tid >> 3, kcb = (tid & 7) * 16, kst = AT_KSWZ(kr, kcb);
;     const int vb0 = (int)(uintptr_t)V_lds + v_rd_base(lane);
;     struct { bf16x8 vs0, vs1, ks0; } sr_[1];
;     const unsigned gvo = (unsigned)((sr * 128 + sc) * 2), gko = (unsigned)((kr * 64 + (tid & 7) * 8) * 2);
;     ...
;     const unsigned cv_ldo = (unsigned)(((tid >> 4) * 2 * 2048 + (tid & 15) * 4) * 4), cv_sto = (unsigned)((tid >> 3) * 2048 + 8 * (tid & 7));
;     const int cv_lw = OFF_CV + (4 * (tid & 15)) * 68 + 2 * (tid >> 4), cv_lr = OFF_CV + (tid >> 3) * 68 + 8 * (tid & 7);
;     f32x4 cvA = f32x4{}, cvB = f32x4{}; unsigned cvr0 = 0, cvr1 = 0;
;     ...
;     f32x16 pA0, pA1, pB0, pB1; float alA, alB; bf16x8 pa0, pa1, pa2, pa3; constexpr int NT = S / 64;
;     constexpr int SE = 0;
;     {
;         bf16x8 v10 = *reinterpret_cast<const bf16x8*>(&Vh[(size_t)(64 + sr) * 128 + sc]), v11 = *reinterpret_cast<const bf16x8*>(&Vh[(size_t)(96 + sr) * 128 + sc]);
;         bf16x8 k10 = *reinterpret_cast<const bf16x8*>(&Kh[(size_t)(64 + kr) * 64 + (tid & 7) * 8]);
;         AT_SLOAD(SE, 0); asm volatile("s_waitcnt vmcnt(0)" ::: "memory");
;         __syncthreads();
;         AT_SWRITE(0, SE);
;         *(bf16x8*)(V_lds + SHM_V + vst0) = v10; *(bf16x8*)(V_lds + SHM_V + vst1) = v11; *(bf16x8*)(K_lds + SHM_K + kst) = k10;
;         __syncthreads();
;     }
;     qkt(pA0, pA1, K_lds, qr, negm, r32, hi); partialSM(pA0, pA1, m_ref, negm, alA);
;     int s_prev = 0, s_cur = 1, s_next = 2;
.LBB4_764:
	v_lshlrev_b32_e32 v24, 4, v22
	v_lshlrev_b32_e32 v23, 3, v22
	v_and_b32_e32 v24, 0xc0, v24
	v_lshlrev_b32_e32 v22, 1, v22
	v_and_or_b32 v24, v23, 24, v24
	v_and_b32_e32 v22, 32, v22
	v_and_b32_e32 v23, 0x100, v23
	s_cmp_lg_u32 0, -1
	v_or3_b32 v202, v24, v22, v23
	s_cselect_b32 s2, 0, 0
	v_add_u32_e32 v192, s2, v202
	s_movk_i32 s2, 0x44
	v_lshl_or_b32 v213, v16, 14, v18
	v_mul_lo_u32 v16, v20, s2
	v_exp_f32_e32 v220, v0
	v_exp_f32_e32 v222, v1
	v_exp_f32_e32 v179, v2
	v_exp_f32_e32 v221, v3
	v_exp_f32_e32 v177, v4
	v_exp_f32_e32 v219, v5
	v_exp_f32_e32 v176, v6
	v_exp_f32_e32 v178, v7
	v_exp_f32_e32 v173, v8
	v_exp_f32_e32 v175, v9
	v_exp_f32_e32 v171, v10
	v_exp_f32_e32 v174, v11
	v_exp_f32_e32 v169, v12
	v_exp_f32_e32 v172, v13
	v_exp_f32_e32 v168, v14
	v_exp_f32_e32 v170, v15
	v_add_u32_e32 v0, 0, v21
	s_mov_b32 s2, 0x22000
	v_add3_u32 v194, v0, v16, s2
	v_add_u32_e32 v0, 0, v19
	v_mov_b32_e32 v162, v183
	v_mov_b32_e32 v163, v183
	v_mov_b32_e32 v48, v183
	v_mov_b32_e32 v49, v183
	v_lshl_or_b32 v193, v20, 11, v21
	v_add3_u32 v195, v0, v17, s2
	v_mov_b32_e32 v182, v183
	v_mov_b32_e32 v160, v183
	v_mov_b32_e32 v161, v183
	v_mov_b32_e32 v50, v183
	v_mov_b32_e32 v51, v183
	v_mov_b32_e32 v52, v183
	v_mov_b32_e32 v53, v183
	v_mov_b32_e32 v54, v183
	v_mov_b32_e32 v55, v183
	v_mov_b32_e32 v56, v183
	v_mov_b32_e32 v57, v183
	v_mov_b32_e32 v58, v183
	v_mov_b32_e32 v59, v183
	v_mov_b32_e32 v60, v183
	v_mov_b32_e32 v61, v183
	v_mov_b32_e32 v62, v183
	v_mov_b32_e32 v63, v183
	v_mov_b64_e32 v[32:33], v[48:49]
	v_mov_b64_e32 v[16:17], v[48:49]
	v_mov_b64_e32 v[0:1], v[48:49]
	v_mov_b64_e32 v[166:167], v[162:163]
	s_mov_b32 s27, 1
	s_mov_b32 s28, 0xc3e00000
	v_mov_b32_e32 v214, 0x43e00000
	s_mov_b32 s20, 0
	v_mov_b64_e32 v[34:35], v[50:51]
	v_mov_b64_e32 v[36:37], v[52:53]
	v_mov_b64_e32 v[38:39], v[54:55]
	v_mov_b64_e32 v[40:41], v[56:57]
	v_mov_b64_e32 v[42:43], v[58:59]
	v_mov_b64_e32 v[44:45], v[60:61]
	v_mov_b64_e32 v[46:47], v[62:63]
	v_mov_b64_e32 v[18:19], v[50:51]
	v_mov_b64_e32 v[20:21], v[52:53]
	v_mov_b64_e32 v[22:23], v[54:55]
	v_mov_b64_e32 v[24:25], v[56:57]
	v_mov_b64_e32 v[26:27], v[58:59]
	v_mov_b64_e32 v[28:29], v[60:61]
	v_mov_b64_e32 v[30:31], v[62:63]
	v_mov_b64_e32 v[2:3], v[50:51]
	v_mov_b64_e32 v[4:5], v[52:53]
	v_mov_b64_e32 v[6:7], v[54:55]
	v_mov_b64_e32 v[8:9], v[56:57]
	v_mov_b64_e32 v[10:11], v[58:59]
	v_mov_b64_e32 v[12:13], v[60:61]
	v_mov_b64_e32 v[14:15], v[62:63]
	v_mov_b64_e32 v[164:165], v[160:161]
	s_mov_b32 s22, 0
	s_mov_b32 s29, 1
	v_mov_b64_e32 v[184:185], v[182:183]
	v_mov_b32_e32 v81, v80
	v_mov_b32_e32 v82, v80
	v_mov_b32_e32 v83, v80
	v_mov_b32_e32 v84, v80
	v_mov_b32_e32 v85, v80
	v_mov_b32_e32 v86, v80
	v_mov_b32_e32 v87, v80
	v_mov_b32_e32 v88, v80
	v_mov_b32_e32 v89, v80
	v_mov_b32_e32 v90, v80
	v_mov_b32_e32 v91, v80
	v_mov_b32_e32 v92, v80
	v_mov_b32_e32 v93, v80
	v_mov_b32_e32 v94, v80
	v_mov_b32_e32 v95, v80
	v_mov_b32_e32 v255, 0x3f600000
	s_mov_b32 s93, 0x3b000000
	v_mbcnt_lo_u32_b32 v253, -1, 0
	v_mbcnt_hi_u32_b32 v253, -1, v253
	v_lshrrev_b32_e32 v253, 5, v253
	v_mul_u32_u24_e32 v253, 0x700, v253
	v_add_u32_e32 v253, v253, v192
	v_mbcnt_lo_u32_b32 v249, -1, 0
	v_mbcnt_hi_u32_b32 v249, -1, v249
	v_bfe_u32 v250, v249, 4, 1
	v_lshlrev_b32_e32 v250, 11, v250
	v_bfe_u32 v251, v249, 2, 2
	v_lshl_add_u32 v250, v251, 8, v250
	v_lshrrev_b32_e32 v251, 5, v249
	v_lshl_add_u32 v250, v251, 6, v250
	v_and_b32_e32 v251, 3, v249
	v_lshl_add_u32 v250, v251, 4, v250
	s_and_b32 s95, s69, 1
	s_lshr_b32 s94, s69, 1
	s_lshl_b32 s94, s94, 12
	s_lshl_b32 s96, s95, 10
	s_add_i32 s94, s94, s96
	v_lshrrev_b32_e32 v251, 4, v249
	v_lshl_add_u32 v251, s95, 2, v251
	v_and_b32_e32 v254, 7, v249
	v_xor_b32_e32 v251, v251, v254
	v_lshlrev_b32_e32 v251, 4, v251
	v_lshrrev_b32_e32 v254, 3, v249
	v_lshl_add_u32 v251, v254, 7, v251
	s_lshl_b32 s96, s69, 10
	v_add_u32_e32 v251, s96, v251
	v_add_u32_e32 v249, s94, v250
	v_add_u32_e32 v250, 0x80, v249
	s_lshl_b32 s94, s69, 11
	s_add_i32 s95, s96, 0xc000
	s_nop 0

; DI void finishSM(f32x16& p0, f32x16& p1, float alpha, float& l_reg, bf16x8& pa0, bf16x8& pa1, bf16x8& pa2, bf16x8& pa3) {
; #pragma unroll
;     for (int r = 0; r < 16; ++r) p1[r] = __builtin_amdgcn_exp2f(p1[r]);
;     float ps = 0;
; #pragma unroll
;     for (int r = 0; r < 16; ++r) ps += p0[r];
; #pragma unroll
;     for (int r = 0; r < 16; ++r) ps += p1[r];
;     { auto rr = __builtin_amdgcn_permlane32_swap(__float_as_uint(ps), __float_as_uint(ps), false, false); ps = __uint_as_float(rr[0]) + __uint_as_float(rr[1]); }
;     l_reg = l_reg * alpha + ps;
;     ...
;     AT_PK4(p0, 0, pa0); AT_PK4(p0, 8, pa1); AT_PK4(p1, 0, pa2); AT_PK4(p1, 8, pa3);
;     ...
; }
; DI void qkt(f32x16& p0, f32x16& p1, const char* Ks, const bf16x8* qr, const f32x16& negm, int r32, int hi) {
; #pragma unroll
;     for (int d0 = 0; d0 < 4; ++d0) { const int cb = (d0 * 16 + hi * 8) * 2;
;         const bf16x8 b0 = *reinterpret_cast<const bf16x8*>(Ks + AT_KSWZ(r32, cb));
;         const bf16x8 b1 = *reinterpret_cast<const bf16x8*>(Ks + AT_KSWZ(32 + r32, cb));
;         p0 = __builtin_amdgcn_mfma_f32_32x32x16_bf16(b0, qr[d0], d0 == 0 ? negm : p0, 0, 0, 0);
;         p1 = __builtin_amdgcn_mfma_f32_32x32x16_bf16(b1, qr[d0], d0 == 0 ? negm : p1, 0, 0, 0); }
; }
.LBB4_775:
	s_lshl_b32 s20, s30, 13
	s_add_i32 s20, s20, 0
	v_add_u32_e32 v72, s20, v208
	v_add_u32_e32 v112, s20, v209
	v_add_u32_e32 v180, s20, v210
	s_waitcnt lgkmcnt(1)
	v_mfma_f32_32x32x16_bf16 v[128:143], v[64:67], v[156:159], v[80:95]
	ds_read_b128 v[64:67], v72 offset:49152
	ds_read_b128 v[72:75], v72 offset:53248
	ds_read_b128 v[76:79], v112 offset:49152
	ds_read_b128 v[224:227], v112 offset:53248
	v_exp_f32_e32 v182, v97
	v_exp_f32_e32 v217, v98
	v_exp_f32_e32 v218, v99
	v_exp_f32_e32 v223, v100
	v_exp_f32_e32 v232, v101
	s_waitcnt lgkmcnt(4)
	v_mfma_f32_32x32x16_bf16 v[112:127], v[68:71], v[156:159], v[80:95]
	ds_read_b128 v[68:71], v180 offset:49152
	ds_read_b128 v[228:231], v180 offset:53248
	v_exp_f32_e32 v180, v96
	v_cvt_pk_bf16_f32 v96, v220, v222
	v_cvt_pk_bf16_f32 v97, v179, v221
	v_cvt_pk_bf16_f32 v98, v177, v219
	v_cvt_pk_bf16_f32 v99, v176, v178
	s_waitcnt lgkmcnt(4)
	v_mfma_f32_32x32x16_bf16 v[112:127], v[72:75], v[152:155], v[112:127]
	v_add_f32_e32 v75, 0, v220
	v_add_f32_e32 v75, v222, v75
	v_add_f32_e32 v75, v179, v75
	v_add_f32_e32 v75, v221, v75
	v_add_f32_e32 v75, v177, v75
	v_add_f32_e32 v75, v219, v75
	v_add_f32_e32 v75, v176, v75
	v_mfma_f32_32x32x16_bf16 v[128:143], v[64:67], v[152:155], v[128:143]
	v_add_f32_e32 v75, v178, v75
	v_add_f32_e32 v75, v173, v75
	v_add_f32_e32 v75, v175, v75
	v_add_f32_e32 v75, v171, v75
	v_add_f32_e32 v75, v174, v75
	v_add_f32_e32 v75, v169, v75
	v_add_f32_e32 v75, v172, v75
	s_waitcnt lgkmcnt(3)
	v_mfma_f32_32x32x16_bf16 v[128:143], v[76:79], v[148:151], v[128:143]
	v_add_f32_e32 v75, v168, v75
	v_add_f32_e32 v75, v170, v75
	v_add_f32_e32 v75, v180, v75
	v_add_f32_e32 v75, v182, v75
	v_exp_f32_e32 v64, v102
	v_exp_f32_e32 v65, v103
	v_exp_f32_e32 v66, v104
	s_waitcnt lgkmcnt(2)
	v_mfma_f32_32x32x16_bf16 v[112:127], v[224:227], v[148:151], v[112:127]
	v_exp_f32_e32 v67, v105
	v_exp_f32_e32 v105, v106
	v_exp_f32_e32 v106, v107
	v_exp_f32_e32 v107, v108
	v_exp_f32_e32 v72, v109
	v_exp_f32_e32 v73, v110
	v_exp_f32_e32 v74, v111
	s_waitcnt lgkmcnt(1)
	v_mfma_f32_32x32x16_bf16 v[128:143], v[68:71], v[144:147], v[128:143]
	v_add_f32_e32 v68, v217, v75
	v_add_f32_e32 v68, v218, v68
	v_add_f32_e32 v68, v223, v68
	v_add_f32_e32 v68, v232, v68
	v_add_f32_e32 v68, v64, v68
	v_add_f32_e32 v68, v65, v68
	v_add_f32_e32 v68, v66, v68
	v_add_f32_e32 v68, v67, v68
	s_waitcnt lgkmcnt(0)
	v_mfma_f32_32x32x16_bf16 v[112:127], v[228:231], v[144:147], v[112:127]
	v_add_f32_e32 v68, v105, v68
	v_add_f32_e32 v68, v106, v68
	v_add_f32_e32 v68, v107, v68
	v_add_f32_e32 v68, v72, v68
	v_add_f32_e32 v68, v73, v68
	v_add_f32_e32 v215, v74, v68
	v_cvt_pk_bf16_f32 v108, v173, v175
	v_cvt_pk_bf16_f32 v109, v171, v174
	v_cvt_pk_bf16_f32 v110, v169, v172
	v_cvt_pk_bf16_f32 v111, v168, v170
	v_cvt_pk_bf16_f32 v100, v180, v182
	v_cvt_pk_bf16_f32 v101, v217, v218
	v_cvt_pk_bf16_f32 v102, v223, v232
	v_cvt_pk_bf16_f32 v103, v64, v65
	v_cvt_pk_bf16_f32 v104, v66, v67
	v_cvt_pk_bf16_f32 v105, v105, v106
	v_cvt_pk_bf16_f32 v106, v107, v72
	v_cvt_pk_bf16_f32 v107, v73, v74
	s_add_u32 s34, s46, s16
	s_addc_u32 s35, s47, s17
	s_add_u32 s24, s34, 0x23808000
	s_addc_u32 s25, s35, 0
	s_add_u32 s66, s34, 0x2380a000
	s_addc_u32 s67, s35, 0
	s_add_u32 s37, s46, s18
	s_addc_u32 s64, s47, s19
	s_add_u32 s74, s37, 0x21884000
	s_addc_u32 s75, s64, 0
	s_lshl_b32 s92, s15, 14
	s_add_i32 s92, s92, s94
	s_mov_b32 m0, s92
	s_lshl_b32 s96, s15, 13
	global_load_lds_dwordx4 v249, s[24:25]
	s_addk_i32 s92, 0x400
	s_mov_b32 m0, s92
	s_add_i32 s96, s96, s95
	global_load_lds_dwordx4 v250, s[24:25]
	s_nop 0
	s_mov_b32 m0, s96
	s_nop 0
	global_load_lds_dwordx4 v251, s[74:75]
	s_andn2_b64 vcc, exec, s[2:3]
	s_cbranch_vccnz .LBB4_777
	s_mov_b64 s[2:3], s[8:9]
	global_store_dwordx2 v193, v[184:185], s[2:3] nt

; #define AT_SBAR() __builtin_amdgcn_sched_barrier(0)
; template <int OFF> DI s16x4 tr_read(int vb) { s16x4 r; asm volatile("ds_read_b64_tr_b16 %0, %1 offset:%2" : "=&v"(r) : "v"(vb), "i"(OFF) : "memory"); return r; }
; template <int D0> DI void pv_one(f32x16& od, int vb, bf16x8 pa0, bf16x8 pa1, bf16x8 pa2, bf16x8 pa3) {
;     const s16x4 l0 = tr_read<v_rd_off(D0, 0, 0)>(vb), h0 = tr_read<v_rd_off(D0, 0, 1)>(vb), l1 = tr_read<v_rd_off(D0, 1, 0)>(vb), h1 = tr_read<v_rd_off(D0, 1, 1)>(vb);
;     const s16x4 l2 = tr_read<v_rd_off(D0, 2, 0)>(vb), h2 = tr_read<v_rd_off(D0, 2, 1)>(vb), l3 = tr_read<v_rd_off(D0, 3, 0)>(vb), h3 = tr_read<v_rd_off(D0, 3, 1)>(vb);
;     asm volatile("s_waitcnt lgkmcnt(0)" ::: "memory"); AT_SBAR();
;     ...
;     od = __builtin_amdgcn_mfma_f32_32x32x16_bf16(AT_PK(l0, h0), pa0, od, 0, 0, 0);
;     od = __builtin_amdgcn_mfma_f32_32x32x16_bf16(AT_PK(l1, h1), pa1, od, 0, 0, 0);
;     od = __builtin_amdgcn_mfma_f32_32x32x16_bf16(AT_PK(l2, h2), pa2, od, 0, 0, 0);
;     od = __builtin_amdgcn_mfma_f32_32x32x16_bf16(AT_PK(l3, h3), pa3, od, 0, 0, 0);
; DI void attn_pass(const Frame& F, CvRide& cv, const bf16_t* __restrict__ Qb, const bf16_t* __restrict__ Kh, const bf16_t* __restrict__ Vh, char* lds, f32x16 (&o)[4], float& l_out, const int wave_s) {
;     ...
;     const unsigned cv_ldo = (unsigned)(((tid >> 4) * 2 * 2048 + (tid & 15) * 4) * 4), cv_sto = (unsigned)((tid >> 3) * 2048 + 8 * (tid & 7));
;     const int cv_lw = OFF_CV + (4 * (tid & 15)) * 68 + 2 * (tid >> 4), cv_lr = OFF_CV + (tid >> 3) * 68 + 8 * (tid & 7);
;     f32x4 cvA = f32x4{}, cvB = f32x4{}; unsigned cvr0 = 0, cvr1 = 0;
.LBB4_779:
	ds_read_b64_tr_b16 v[218:219], v182 offset:0x600
	ds_read_b64_tr_b16 v[220:221], v182 offset:0x700
	ds_read_b64_tr_b16 v[222:223], v182 offset:0x1600
	ds_read_b64_tr_b16 v[224:225], v182 offset:0x1700
	ds_read_b64_tr_b16 v[226:227], v182 offset:0x2600
	ds_read_b64_tr_b16 v[228:229], v182 offset:0x2700
	ds_read_b64_tr_b16 v[230:231], v182 offset:0x3600
	ds_read_b64_tr_b16 v[232:233], v182 offset:0x3700
	s_waitcnt lgkmcnt(0)
	v_mfma_f32_32x32x16_bf16 v[0:15], v[218:221], v[96:99], v[0:15]
	s_lshl_b32 s2, s15, 14
	s_lshl_b32 s3, s15, 13
	s_sub_i32 s65, s2, s3
	s_waitcnt vmcnt(3)
	v_mfma_f32_32x32x16_bf16 v[0:15], v[222:225], v[108:111], v[0:15]
	s_andn2_b64 s[2:3], exec, s[22:23]
	s_andn2_b64 vcc, exec, s[22:23]
	v_mfma_f32_32x32x16_bf16 v[0:15], v[226:229], v[100:103], v[0:15]
	v_mfma_f32_32x32x16_bf16 v[0:15], v[230:233], v[104:107], v[0:15]
	s_cbranch_vccnz .LBB4_784
	v_med3_f32 v97, v160, -v255, v255
	v_med3_f32 v98, v164, -v255, v255
	v_cvt_scalef32_pk_fp8_f32 v99, v97, v98, s93
	v_med3_f32 v97, v161, -v255, v255
	v_med3_f32 v98, v165, -v255, v255
	v_cvt_scalef32_pk_fp8_f32 v100, v97, v98, s93
	v_med3_f32 v97, v162, -v255, v255
	v_med3_f32 v98, v166, -v255, v255
	s_bitcmp1_b32 s58, 0
	v_cvt_scalef32_pk_fp8_f32 v101, v97, v98, s93
	s_cselect_b32 s8, 0x1100, 0
	v_med3_f32 v97, v163, -v255, v255
	v_med3_f32 v98, v167, -v255, v255
	v_cmp_eq_u32_e32 vcc, 0, v181
	v_add_u32_e32 v96, s8, v195
	v_cvt_scalef32_pk_fp8_f32 v102, v97, v98, s93
	s_and_b64 vcc, exec, vcc
	s_and_b32 s22, s58, 31
	ds_write_b16 v96, v99
	ds_write_b16 v96, v100 offset:68
	ds_write_b16 v96, v101 offset:136
	ds_write_b16 v96, v102 offset:204
	s_cbranch_vccnz .LBB4_808
	s_lshl_b32 s8, s22, 7
	s_lshl_b32 s9, s58, 6
	s_and_b32 s8, s8, 0xf00
	s_and_b32 s9, s9, 64
	s_or_b32 s20, s8, s9
	s_cbranch_execnz .LBB4_783

.LBB4_786:
	s_and_b64 vcc, exec, s[2:3]
	s_waitcnt vmcnt(0) lgkmcnt(0)
	s_barrier
	v_add_u32_e32 v100, s65, v207
	ds_read_b128 v[96:99], v100 offset:49152
	ds_read_b128 v[168:171], v100 offset:53248
	s_cbranch_vccnz .LBB4_788
	s_andn2_b32 s20, 1, s58
	s_mulk_i32 s20, 0x1100
	v_add_u32_e32 v252, s20, v194
	ds_read2_b32 v[184:185], v252 offset1:1

; DI void finishSM(f32x16& p0, f32x16& p1, float alpha, float& l_reg, bf16x8& pa0, bf16x8& pa1, bf16x8& pa2, bf16x8& pa3) {
; #pragma unroll
;     for (int r = 0; r < 16; ++r) p1[r] = __builtin_amdgcn_exp2f(p1[r]);
;     float ps = 0;
; #pragma unroll
;     for (int r = 0; r < 16; ++r) ps += p0[r];
; #pragma unroll
;     for (int r = 0; r < 16; ++r) ps += p1[r];
;     { auto rr = __builtin_amdgcn_permlane32_swap(__float_as_uint(ps), __float_as_uint(ps), false, false); ps = __uint_as_float(rr[0]) + __uint_as_float(rr[1]); }
;     l_reg = l_reg * alpha + ps;
;     ...
;     AT_PK4(p0, 0, pa0); AT_PK4(p0, 8, pa1); AT_PK4(p1, 0, pa2); AT_PK4(p1, 8, pa3);
;     ...
; }
; DI void qkt(f32x16& p0, f32x16& p1, const char* Ks, const bf16x8* qr, const f32x16& negm, int r32, int hi) {
; #pragma unroll
;     for (int d0 = 0; d0 < 4; ++d0) { const int cb = (d0 * 16 + hi * 8) * 2;
;         const bf16x8 b0 = *reinterpret_cast<const bf16x8*>(Ks + AT_KSWZ(r32, cb));
;         const bf16x8 b1 = *reinterpret_cast<const bf16x8*>(Ks + AT_KSWZ(32 + r32, cb));
;         p0 = __builtin_amdgcn_mfma_f32_32x32x16_bf16(b0, qr[d0], d0 == 0 ? negm : p0, 0, 0, 0);
;         p1 = __builtin_amdgcn_mfma_f32_32x32x16_bf16(b1, qr[d0], d0 == 0 ? negm : p1, 0, 0, 0); }
; }
.LBB4_796:
	v_exp_f32_e32 v182, v128
	v_exp_f32_e32 v234, v129
	v_exp_f32_e32 v235, v130
	v_exp_f32_e32 v236, v131
	v_exp_f32_e32 v237, v132
	v_exp_f32_e32 v238, v133
	v_exp_f32_e32 v239, v134
	v_exp_f32_e32 v240, v135
	v_exp_f32_e32 v241, v136
	v_exp_f32_e32 v242, v137
	v_exp_f32_e32 v243, v138
	v_exp_f32_e32 v244, v139
	v_exp_f32_e32 v245, v140
	v_exp_f32_e32 v246, v141
	v_exp_f32_e32 v247, v142
	v_exp_f32_e32 v248, v143
	v_add_u32_e32 v101, s65, v208
	v_add_u32_e32 v102, s65, v209
	v_add_u32_e32 v103, s65, v210
	ds_read_b128 v[172:175], v101 offset:49152
	ds_read_b128 v[176:179], v101 offset:53248
	ds_read_b128 v[218:221], v102 offset:49152
	ds_read_b128 v[222:225], v102 offset:53248
	ds_read_b128 v[226:229], v103 offset:49152
	ds_read_b128 v[230:233], v103 offset:53248
	v_exp_f32_e32 v112, v112
	v_exp_f32_e32 v113, v113
	v_exp_f32_e32 v114, v114
	s_waitcnt lgkmcnt(7)
	v_mfma_f32_32x32x16_bf16 v[128:143], v[96:99], v[156:159], v[80:95]
	v_exp_f32_e32 v115, v115
	v_exp_f32_e32 v116, v116
	v_exp_f32_e32 v117, v117
	v_exp_f32_e32 v118, v118
	v_exp_f32_e32 v119, v119
	s_waitcnt lgkmcnt(6)
	v_mfma_f32_32x32x16_bf16 v[96:111], v[168:171], v[156:159], v[80:95]
	v_exp_f32_e32 v168, v120
	v_add_f32_e32 v120, 0, v182
	v_add_f32_e32 v120, v234, v120
	v_add_f32_e32 v120, v235, v120
	v_add_f32_e32 v120, v236, v120
	v_add_f32_e32 v120, v237, v120
	v_add_f32_e32 v120, v238, v120
	v_add_f32_e32 v120, v239, v120
	v_add_f32_e32 v120, v240, v120
	v_add_f32_e32 v120, v241, v120
	v_add_f32_e32 v120, v242, v120
	s_waitcnt lgkmcnt(5)
	v_mfma_f32_32x32x16_bf16 v[128:143], v[172:175], v[152:155], v[128:143]
	v_add_f32_e32 v120, v243, v120
	v_add_f32_e32 v120, v244, v120
	v_add_f32_e32 v120, v245, v120
	v_add_f32_e32 v120, v246, v120
	v_add_f32_e32 v120, v247, v120
	v_add_f32_e32 v120, v248, v120
	v_add_f32_e32 v120, v112, v120
	s_waitcnt lgkmcnt(4)
	v_mfma_f32_32x32x16_bf16 v[96:111], v[176:179], v[152:155], v[96:111]
	v_add_f32_e32 v120, v113, v120
	v_add_f32_e32 v120, v114, v120
	v_add_f32_e32 v120, v115, v120
	v_add_f32_e32 v120, v116, v120
	v_exp_f32_e32 v169, v121
	v_add_f32_e32 v120, v117, v120
	v_exp_f32_e32 v170, v122
	s_waitcnt lgkmcnt(3)
	v_mfma_f32_32x32x16_bf16 v[128:143], v[218:221], v[148:151], v[128:143]
	v_add_f32_e32 v120, v118, v120
	v_exp_f32_e32 v171, v123
	v_add_f32_e32 v120, v119, v120
	v_exp_f32_e32 v172, v124
	v_add_f32_e32 v120, v168, v120
	v_exp_f32_e32 v173, v125
	v_add_f32_e32 v120, v169, v120
	s_waitcnt lgkmcnt(2)
	v_mfma_f32_32x32x16_bf16 v[96:111], v[222:225], v[148:151], v[96:111]
	v_exp_f32_e32 v174, v126
	v_add_f32_e32 v120, v170, v120
	v_exp_f32_e32 v175, v127
	v_add_f32_e32 v120, v171, v120
	v_add_f32_e32 v120, v172, v120
	v_add_f32_e32 v120, v173, v120
	v_add_f32_e32 v120, v174, v120
	s_waitcnt lgkmcnt(1)
	v_mfma_f32_32x32x16_bf16 v[128:143], v[226:229], v[144:147], v[128:143]
	v_add_f32_e32 v217, v175, v120
	v_cvt_pk_bf16_f32 v120, v182, v234
	v_cvt_pk_bf16_f32 v121, v235, v236
	v_cvt_pk_bf16_f32 v122, v237, v238
	v_cvt_pk_bf16_f32 v123, v239, v240
	v_cvt_pk_bf16_f32 v124, v241, v242
	s_waitcnt lgkmcnt(0)
	v_mfma_f32_32x32x16_bf16 v[96:111], v[230:233], v[144:147], v[96:111]
	v_cvt_pk_bf16_f32 v125, v243, v244
	v_cvt_pk_bf16_f32 v126, v245, v246
	v_cvt_pk_bf16_f32 v127, v247, v248
	v_cvt_pk_bf16_f32 v112, v112, v113
	v_cvt_pk_bf16_f32 v113, v114, v115
	v_cvt_pk_bf16_f32 v114, v116, v117
	v_cvt_pk_bf16_f32 v115, v118, v119
	v_cvt_pk_bf16_f32 v116, v168, v169
	v_cvt_pk_bf16_f32 v117, v170, v171
	v_cvt_pk_bf16_f32 v118, v172, v173
	v_cvt_pk_bf16_f32 v119, v174, v175
	s_add_u32 s24, s34, 0x2380c000
	s_addc_u32 s25, s35, 0
	s_add_u32 s34, s34, 0x2380e000
	s_addc_u32 s35, s35, 0
	s_add_u32 s66, s37, 0x21886000
	s_addc_u32 s67, s64, 0
	s_lshl_b32 s92, s29, 14
	s_add_i32 s92, s92, s94
	s_mov_b32 m0, s92
	s_lshl_b32 s96, s29, 13
	global_load_lds_dwordx4 v249, s[24:25]
	s_addk_i32 s92, 0x400
	s_mov_b32 m0, s92
	s_add_i32 s96, s96, s95
	global_load_lds_dwordx4 v250, s[24:25]
	s_nop 0
	s_mov_b32 m0, s96
	s_nop 0
	global_load_lds_dwordx4 v251, s[66:67]
	s_nop 0
	s_and_b64 vcc, exec, s[2:3]
	s_cbranch_vccnz .LBB4_798
	s_mov_b64 s[2:3], s[8:9]
	global_store_dwordx2 v193, v[184:185], s[2:3] nt

; #define AT_SBAR() __builtin_amdgcn_sched_barrier(0)
; template <int OFF> DI s16x4 tr_read(int vb) { s16x4 r; asm volatile("ds_read_b64_tr_b16 %0, %1 offset:%2" : "=&v"(r) : "v"(vb), "i"(OFF) : "memory"); return r; }
; template <int D0> DI void pv_one(f32x16& od, int vb, bf16x8 pa0, bf16x8 pa1, bf16x8 pa2, bf16x8 pa3) {
;     const s16x4 l0 = tr_read<v_rd_off(D0, 0, 0)>(vb), h0 = tr_read<v_rd_off(D0, 0, 1)>(vb), l1 = tr_read<v_rd_off(D0, 1, 0)>(vb), h1 = tr_read<v_rd_off(D0, 1, 1)>(vb);
;     const s16x4 l2 = tr_read<v_rd_off(D0, 2, 0)>(vb), h2 = tr_read<v_rd_off(D0, 2, 1)>(vb), l3 = tr_read<v_rd_off(D0, 3, 0)>(vb), h3 = tr_read<v_rd_off(D0, 3, 1)>(vb);
;     asm volatile("s_waitcnt lgkmcnt(0)" ::: "memory"); AT_SBAR();
;     ...
;     od = __builtin_amdgcn_mfma_f32_32x32x16_bf16(AT_PK(l0, h0), pa0, od, 0, 0, 0);
;     od = __builtin_amdgcn_mfma_f32_32x32x16_bf16(AT_PK(l1, h1), pa1, od, 0, 0, 0);
;     od = __builtin_amdgcn_mfma_f32_32x32x16_bf16(AT_PK(l2, h2), pa2, od, 0, 0, 0);
;     od = __builtin_amdgcn_mfma_f32_32x32x16_bf16(AT_PK(l3, h3), pa3, od, 0, 0, 0);
; DI void attn_pass(const Frame& F, CvRide& cv, const bf16_t* __restrict__ Qb, const bf16_t* __restrict__ Kh, const bf16_t* __restrict__ Vh, char* lds, f32x16 (&o)[4], float& l_out, const int wave_s) {
;     ...
;     const unsigned cv_ldo = (unsigned)(((tid >> 4) * 2 * 2048 + (tid & 15) * 4) * 4), cv_sto = (unsigned)((tid >> 3) * 2048 + 8 * (tid & 7));
;     const int cv_lw = OFF_CV + (4 * (tid & 15)) * 68 + 2 * (tid >> 4), cv_lr = OFF_CV + (tid >> 3) * 68 + 8 * (tid & 7);
;     f32x4 cvA = f32x4{}, cvB = f32x4{}; unsigned cvr0 = 0, cvr1 = 0;
.LBB4_799:
	ds_read_b64_tr_b16 v[220:221], v219 offset:0x600
	ds_read_b64_tr_b16 v[222:223], v219 offset:0x700
	ds_read_b64_tr_b16 v[224:225], v219 offset:0x1600
	ds_read_b64_tr_b16 v[226:227], v219 offset:0x1700
	ds_read_b64_tr_b16 v[228:229], v219 offset:0x2600
	ds_read_b64_tr_b16 v[230:231], v219 offset:0x2700
	ds_read_b64_tr_b16 v[232:233], v219 offset:0x3600
	ds_read_b64_tr_b16 v[234:235], v219 offset:0x3700
	s_waitcnt lgkmcnt(0)
	v_mfma_f32_32x32x16_bf16 v[0:15], v[220:223], v[120:123], v[0:15]
	s_add_i32 s2, s31, 0
	s_waitcnt vmcnt(3)
	s_mov_b32 s20, 0
	s_andn2_b64 vcc, exec, s[22:23]
	v_mfma_f32_32x32x16_bf16 v[0:15], v[224:227], v[124:127], v[0:15]
	v_mfma_f32_32x32x16_bf16 v[0:15], v[228:231], v[112:115], v[0:15]
	s_andn2_b64 s[2:3], exec, s[22:23]
	v_mfma_f32_32x32x16_bf16 v[0:15], v[232:235], v[116:119], v[0:15]
	s_cbranch_vccnz .LBB4_804
	v_med3_f32 v113, v160, -v255, v255
	v_med3_f32 v114, v164, -v255, v255
	v_cvt_scalef32_pk_fp8_f32 v115, v113, v114, s93
	v_med3_f32 v113, v161, -v255, v255
	v_med3_f32 v114, v165, -v255, v255
	v_cvt_scalef32_pk_fp8_f32 v116, v113, v114, s93
	v_med3_f32 v113, v162, -v255, v255
	v_med3_f32 v114, v166, -v255, v255
	s_bitcmp1_b32 s58, 0
	v_cvt_scalef32_pk_fp8_f32 v117, v113, v114, s93
	s_cselect_b32 s8, 0x1100, 0
	v_med3_f32 v113, v163, -v255, v255
	v_med3_f32 v114, v167, -v255, v255
	v_cmp_eq_u32_e32 vcc, 0, v181
	v_add_u32_e32 v112, s8, v195
	v_cvt_scalef32_pk_fp8_f32 v118, v113, v114, s93
	s_and_b64 vcc, exec, vcc
	s_and_b32 s24, s58, 31
	ds_write_b16 v112, v115
	ds_write_b16 v112, v116 offset:68
	ds_write_b16 v112, v117 offset:136
	ds_write_b16 v112, v118 offset:204
	s_cbranch_vccnz .LBB4_809
	s_lshl_b32 s8, s24, 7
	s_lshl_b32 s9, s58, 6
	s_and_b32 s8, s8, 0xf00
	s_and_b32 s9, s9, 64
	s_or_b32 s20, s8, s9
	s_cbranch_execnz .LBB4_803

; DI void pv_all_sm(f32x16* o, int vb, bf16x8 pa0, bf16x8 pa1, bf16x8 pa2, bf16x8 pa3, f32x16& p0, f32x16& p1, float& m_ref, f32x16& negm, float& alpha) {
;     ...
; #pragma unroll
;     for (int r = 0; r < 16; ++r) p0[r] = __builtin_amdgcn_exp2f(p0[r]);
; DI void attn_pass(const Frame& F, CvRide& cv, const bf16_t* __restrict__ Qb, const bf16_t* __restrict__ Kh, const bf16_t* __restrict__ Vh, char* lds, f32x16 (&o)[4], float& l_out, const int wave_s) {
;     ...
;     for (int j = 1; j + 2 < NT; j += 2) {
;         AT_STEP(pB0, pB1, pA0, pA1, alB, alA, j, true);
;         AT_STEP(pA0, pA1, pB0, pB1, alA, alB, j + 1, true);
;     }
.LBB4_806:
	s_add_u32 s18, s18, 0x4000
	v_exp_f32_e32 v220, v128
	v_exp_f32_e32 v222, v129
	v_exp_f32_e32 v179, v130
	v_exp_f32_e32 v221, v131
	v_exp_f32_e32 v177, v132
	v_exp_f32_e32 v219, v133
	v_exp_f32_e32 v176, v134
	v_exp_f32_e32 v178, v135
	v_exp_f32_e32 v173, v136
	v_exp_f32_e32 v175, v137
	v_exp_f32_e32 v171, v138
	v_exp_f32_e32 v174, v139
	v_exp_f32_e32 v169, v140
	v_exp_f32_e32 v172, v141
	v_exp_f32_e32 v168, v142
	v_exp_f32_e32 v170, v143
	s_addc_u32 s19, s19, 0
	s_add_u32 s16, s16, 0x8000
	v_fma_f32 v112, v211, v183, v215
	s_addc_u32 s17, s17, 0
	s_add_i32 s27, s27, 2
	v_fma_f32 v183, v112, v180, v217
	s_cmp_gt_u32 s27, 61
	s_waitcnt vmcnt(0) lgkmcnt(0)
	s_barrier
	s_cbranch_scc1 .LBB4_812
	s_mov_b32 s22, s15
	s_mov_b32 s15, s30
	v_mov_b32_e32 v211, v182
	s_branch .LBB4_765

; DI int tid_fresh(int wave) { return wave * 64 + lane_fresh(); }
; DI void attn_pass(const Frame& F, CvRide& cv, const bf16_t* __restrict__ Qb, const bf16_t* __restrict__ Kh, const bf16_t* __restrict__ Vh, char* lds, f32x16 (&o)[4], float& l_out, const int wave_s) {
;     const int tid = tid_fresh(wave_s), wid = tid >> 6, lane = tid & 63, r32 = lane & 31, hi = lane >> 5;
;     char* V_lds = lds + OFF_V; char* K_lds = lds + OFF_K;
;     float m_ref = 0.f, l_reg = 0.f; bf16x8 qr[4]; f32x16 negm = f32x16{};
; #pragma unroll
;     for (int d = 0; d < 4; ++d) o[d] = f32x16{};
;     const bf16_t* Qw = Qb + (size_t)(wid * 32 + r32) * 64 + hi * 8;
; #pragma unroll
;     for (int d0 = 0; d0 < 4; ++d0) qr[d0] = *reinterpret_cast<const bf16x8*>(Qw + d0 * 16);
;     const int sr = tid >> 4, sc = (tid & 15) * 8, vst0 = v_st(sr, sc), vst1 = v_st(32 + sr, sc);
;     const int kr = tid >> 3, kcb = (tid & 7) * 16, kst = AT_KSWZ(kr, kcb);
;     const int vb0 = (int)(uintptr_t)V_lds + v_rd_base(lane);
;     struct { bf16x8 vs0, vs1, ks0; } sr_[1];
;     const unsigned gvo = (unsigned)((sr * 128 + sc) * 2), gko = (unsigned)((kr * 64 + (tid & 7) * 8) * 2);
;     ...
;     const unsigned cv_ldo = (unsigned)(((tid >> 4) * 2 * 2048 + (tid & 15) * 4) * 4), cv_sto = (unsigned)((tid >> 3) * 2048 + 8 * (tid & 7));
;     const int cv_lw = OFF_CV + (4 * (tid & 15)) * 68 + 2 * (tid >> 4), cv_lr = OFF_CV + (tid >> 3) * 68 + 8 * (tid & 7);
;     f32x4 cvA = f32x4{}, cvB = f32x4{}; unsigned cvr0 = 0, cvr1 = 0;
;     ...
;     f32x16 pA0, pA1, pB0, pB1; float alA, alB; bf16x8 pa0, pa1, pa2, pa3; constexpr int NT = S / 64;
;     constexpr int SE = 0;
;     {
;         bf16x8 v10 = *reinterpret_cast<const bf16x8*>(&Vh[(size_t)(64 + sr) * 128 + sc]), v11 = *reinterpret_cast<const bf16x8*>(&Vh[(size_t)(96 + sr) * 128 + sc]);
;         bf16x8 k10 = *reinterpret_cast<const bf16x8*>(&Kh[(size_t)(64 + kr) * 64 + (tid & 7) * 8]);
;         AT_SLOAD(SE, 0); asm volatile("s_waitcnt vmcnt(0)" ::: "memory");
;         __syncthreads();
;         AT_SWRITE(0, SE);
;         *(bf16x8*)(V_lds + SHM_V + vst0) = v10; *(bf16x8*)(V_lds + SHM_V + vst1) = v11; *(bf16x8*)(K_lds + SHM_K + kst) = k10;
;         __syncthreads();
;     }
;     qkt(pA0, pA1, K_lds, qr, negm, r32, hi); partialSM(pA0, pA1, m_ref, negm, alA);
;     int s_prev = 0, s_cur = 1, s_next = 2;
.LBB4_838:
	v_lshlrev_b32_e32 v24, 4, v22
	v_lshlrev_b32_e32 v23, 3, v22
	v_and_b32_e32 v24, 0xc0, v24
	v_lshlrev_b32_e32 v22, 1, v22
	v_and_or_b32 v24, v23, 24, v24
	v_and_b32_e32 v22, 32, v22
	v_and_b32_e32 v23, 0x100, v23
	s_cmp_lg_u32 0, -1
	v_or3_b32 v198, v24, v22, v23
	s_cselect_b32 s2, 0, 0
	v_add_u32_e32 v191, s2, v198
	s_movk_i32 s2, 0x44
	v_lshl_or_b32 v209, v16, 14, v18
	v_mul_lo_u32 v16, v20, s2
	v_exp_f32_e32 v216, v0
	v_exp_f32_e32 v218, v1
	v_exp_f32_e32 v179, v2
	v_exp_f32_e32 v217, v3
	v_exp_f32_e32 v177, v4
	v_exp_f32_e32 v215, v5
	v_exp_f32_e32 v176, v6
	v_exp_f32_e32 v178, v7
	v_exp_f32_e32 v173, v8
	v_exp_f32_e32 v175, v9
	v_exp_f32_e32 v171, v10
	v_exp_f32_e32 v174, v11
	v_exp_f32_e32 v169, v12
	v_exp_f32_e32 v172, v13
	v_exp_f32_e32 v168, v14
	v_exp_f32_e32 v170, v15
	v_add_u32_e32 v0, 0, v21
	s_mov_b32 s2, 0x22000
	v_add3_u32 v189, v0, v16, s2
	v_add_u32_e32 v0, 0, v19
	v_mov_b32_e32 v162, v183
	v_mov_b32_e32 v163, v183
	v_mov_b32_e32 v32, v183
	v_mov_b32_e32 v33, v183
	v_mov_b32_e32 v46, v183
	v_mov_b32_e32 v47, v183
	v_lshl_or_b32 v188, v20, 11, v21
	v_add3_u32 v190, v0, v17, s2
	v_mov_b32_e32 v182, v183
	v_mov_b32_e32 v160, v183
	v_mov_b32_e32 v161, v183
	v_mov_b32_e32 v34, v183
	v_mov_b32_e32 v35, v183
	v_mov_b32_e32 v36, v183
	v_mov_b32_e32 v37, v183
	v_mov_b32_e32 v38, v183
	v_mov_b32_e32 v39, v183
	v_mov_b32_e32 v40, v183
	v_mov_b32_e32 v41, v183
	v_mov_b32_e32 v42, v183
	v_mov_b32_e32 v43, v183
	v_mov_b32_e32 v44, v183
	v_mov_b32_e32 v45, v183
	v_mov_b64_e32 v[62:63], v[46:47]
	v_mov_b64_e32 v[16:17], v[32:33]
	v_mov_b64_e32 v[0:1], v[32:33]
	v_mov_b64_e32 v[166:167], v[162:163]
	s_mov_b32 s23, 1
	s_mov_b32 s57, 2
	s_mov_b32 s56, 0xc3e00000
	v_mov_b32_e32 v210, 0x43e00000
	s_mov_b64 s[28:29], s[16:17]
	s_mov_b32 s26, 0
	v_mov_b64_e32 v[60:61], v[44:45]
	v_mov_b64_e32 v[58:59], v[42:43]
	v_mov_b64_e32 v[56:57], v[40:41]
	v_mov_b64_e32 v[54:55], v[38:39]
	v_mov_b64_e32 v[52:53], v[36:37]
	v_mov_b64_e32 v[50:51], v[34:35]
	v_mov_b64_e32 v[48:49], v[32:33]
	v_mov_b64_e32 v[18:19], v[34:35]
	v_mov_b64_e32 v[20:21], v[36:37]
	v_mov_b64_e32 v[22:23], v[38:39]
	v_mov_b64_e32 v[24:25], v[40:41]
	v_mov_b64_e32 v[26:27], v[42:43]
	v_mov_b64_e32 v[28:29], v[44:45]
	v_mov_b64_e32 v[30:31], v[46:47]
	v_mov_b64_e32 v[2:3], v[34:35]
	v_mov_b64_e32 v[4:5], v[36:37]
	v_mov_b64_e32 v[6:7], v[38:39]
	v_mov_b64_e32 v[8:9], v[40:41]
	v_mov_b64_e32 v[10:11], v[42:43]
	v_mov_b64_e32 v[12:13], v[44:45]
	v_mov_b64_e32 v[14:15], v[46:47]
	v_mov_b64_e32 v[164:165], v[160:161]
	s_mov_b32 s30, 0
	s_mov_b32 s63, 1
	v_mov_b64_e32 v[184:185], v[182:183]
	v_mov_b32_e32 v81, v80
	v_mov_b32_e32 v82, v80
	v_mov_b32_e32 v83, v80
	v_mov_b32_e32 v84, v80
	v_mov_b32_e32 v85, v80
	v_mov_b32_e32 v86, v80
	v_mov_b32_e32 v87, v80
	v_mov_b32_e32 v88, v80
	v_mov_b32_e32 v89, v80
	v_mov_b32_e32 v90, v80
	v_mov_b32_e32 v91, v80
	v_mov_b32_e32 v92, v80
	v_mov_b32_e32 v93, v80
	v_mov_b32_e32 v94, v80
	v_mov_b32_e32 v95, v80
	v_mov_b32_e32 v255, 0x3f600000
	s_mov_b32 s93, 0x3b000000
	v_mbcnt_lo_u32_b32 v253, -1, 0
	v_mbcnt_hi_u32_b32 v253, -1, v253
	v_lshrrev_b32_e32 v253, 5, v253
	v_mul_u32_u24_e32 v253, 0x700, v253
	v_add_u32_e32 v253, v253, v191
	v_mbcnt_lo_u32_b32 v249, -1, 0
	v_mbcnt_hi_u32_b32 v249, -1, v249
	v_bfe_u32 v250, v249, 4, 1
	v_lshlrev_b32_e32 v250, 11, v250
	v_bfe_u32 v251, v249, 2, 2
	v_lshl_add_u32 v250, v251, 8, v250
	v_lshrrev_b32_e32 v251, 5, v249
	v_lshl_add_u32 v250, v251, 6, v250
	v_and_b32_e32 v251, 3, v249
	v_lshl_add_u32 v250, v251, 4, v250
	s_and_b32 s95, s69, 1
	s_lshr_b32 s94, s69, 1
	s_lshl_b32 s94, s94, 12
	s_lshl_b32 s96, s95, 10
	s_add_i32 s94, s94, s96
	v_lshrrev_b32_e32 v251, 4, v249
	v_lshl_add_u32 v251, s95, 2, v251
	v_and_b32_e32 v254, 7, v249
	v_xor_b32_e32 v251, v251, v254
	v_lshlrev_b32_e32 v251, 4, v251
	v_lshrrev_b32_e32 v254, 3, v249
	v_lshl_add_u32 v251, v254, 7, v251
	s_lshl_b32 s96, s69, 10
	v_add_u32_e32 v251, s96, v251
	v_add_u32_e32 v249, s94, v250
	v_add_u32_e32 v250, 0x80, v249
	s_lshl_b32 s94, s69, 11
	s_add_i32 s95, s96, 0xc000
	s_nop 0

; DI void finishSM(f32x16& p0, f32x16& p1, float alpha, float& l_reg, bf16x8& pa0, bf16x8& pa1, bf16x8& pa2, bf16x8& pa3) {
; #pragma unroll
;     for (int r = 0; r < 16; ++r) p1[r] = __builtin_amdgcn_exp2f(p1[r]);
;     float ps = 0;
; #pragma unroll
;     for (int r = 0; r < 16; ++r) ps += p0[r];
; #pragma unroll
;     for (int r = 0; r < 16; ++r) ps += p1[r];
;     { auto rr = __builtin_amdgcn_permlane32_swap(__float_as_uint(ps), __float_as_uint(ps), false, false); ps = __uint_as_float(rr[0]) + __uint_as_float(rr[1]); }
;     l_reg = l_reg * alpha + ps;
;     ...
;     AT_PK4(p0, 0, pa0); AT_PK4(p0, 8, pa1); AT_PK4(p1, 0, pa2); AT_PK4(p1, 8, pa3);
;     ...
; }
; DI void qkt(f32x16& p0, f32x16& p1, const char* Ks, const bf16x8* qr, const f32x16& negm, int r32, int hi) {
; #pragma unroll
;     for (int d0 = 0; d0 < 4; ++d0) { const int cb = (d0 * 16 + hi * 8) * 2;
;         const bf16x8 b0 = *reinterpret_cast<const bf16x8*>(Ks + AT_KSWZ(r32, cb));
;         const bf16x8 b1 = *reinterpret_cast<const bf16x8*>(Ks + AT_KSWZ(32 + r32, cb));
;         p0 = __builtin_amdgcn_mfma_f32_32x32x16_bf16(b0, qr[d0], d0 == 0 ? negm : p0, 0, 0, 0);
;         p1 = __builtin_amdgcn_mfma_f32_32x32x16_bf16(b1, qr[d0], d0 == 0 ? negm : p1, 0, 0, 0); }
; }
.LBB4_849:
	s_lshl_b32 s26, s64, 13
	s_add_i32 s26, s26, 0
	v_add_u32_e32 v72, s26, v204
	v_add_u32_e32 v112, s26, v205
	v_add_u32_e32 v180, s26, v206
	s_waitcnt lgkmcnt(1)
	v_mfma_f32_32x32x16_bf16 v[128:143], v[64:67], v[156:159], v[80:95]
	ds_read_b128 v[64:67], v72 offset:49152
	ds_read_b128 v[72:75], v72 offset:53248
	ds_read_b128 v[76:79], v112 offset:49152
	ds_read_b128 v[220:223], v112 offset:53248
	v_exp_f32_e32 v182, v97
	v_exp_f32_e32 v213, v98
	v_exp_f32_e32 v214, v99
	v_exp_f32_e32 v219, v100
	v_exp_f32_e32 v228, v101
	s_waitcnt lgkmcnt(4)
	v_mfma_f32_32x32x16_bf16 v[112:127], v[68:71], v[156:159], v[80:95]
	ds_read_b128 v[68:71], v180 offset:49152
	ds_read_b128 v[224:227], v180 offset:53248
	v_exp_f32_e32 v180, v96
	v_cvt_pk_bf16_f32 v96, v216, v218
	v_cvt_pk_bf16_f32 v97, v179, v217
	v_cvt_pk_bf16_f32 v98, v177, v215
	v_cvt_pk_bf16_f32 v99, v176, v178
	s_waitcnt lgkmcnt(4)
	v_mfma_f32_32x32x16_bf16 v[112:127], v[72:75], v[152:155], v[112:127]
	v_add_f32_e32 v75, 0, v216
	v_add_f32_e32 v75, v218, v75
	v_add_f32_e32 v75, v179, v75
	v_add_f32_e32 v75, v217, v75
	v_add_f32_e32 v75, v177, v75
	v_add_f32_e32 v75, v215, v75
	v_add_f32_e32 v75, v176, v75
	v_mfma_f32_32x32x16_bf16 v[128:143], v[64:67], v[152:155], v[128:143]
	v_add_f32_e32 v75, v178, v75
	v_add_f32_e32 v75, v173, v75
	v_add_f32_e32 v75, v175, v75
	v_add_f32_e32 v75, v171, v75
	v_add_f32_e32 v75, v174, v75
	v_add_f32_e32 v75, v169, v75
	v_add_f32_e32 v75, v172, v75
	s_waitcnt lgkmcnt(3)
	v_mfma_f32_32x32x16_bf16 v[128:143], v[76:79], v[148:151], v[128:143]
	v_add_f32_e32 v75, v168, v75
	v_add_f32_e32 v75, v170, v75
	v_add_f32_e32 v75, v180, v75
	v_add_f32_e32 v75, v182, v75
	v_exp_f32_e32 v64, v102
	v_exp_f32_e32 v65, v103
	v_exp_f32_e32 v66, v104
	s_waitcnt lgkmcnt(2)
	v_mfma_f32_32x32x16_bf16 v[112:127], v[220:223], v[148:151], v[112:127]
	v_exp_f32_e32 v67, v105
	v_exp_f32_e32 v105, v106
	v_exp_f32_e32 v106, v107
	v_exp_f32_e32 v107, v108
	v_exp_f32_e32 v72, v109
	v_exp_f32_e32 v73, v110
	v_exp_f32_e32 v74, v111
	s_waitcnt lgkmcnt(1)
	v_mfma_f32_32x32x16_bf16 v[128:143], v[68:71], v[144:147], v[128:143]
	v_add_f32_e32 v68, v213, v75
	v_add_f32_e32 v68, v214, v68
	v_add_f32_e32 v68, v219, v68
	v_add_f32_e32 v68, v228, v68
	v_add_f32_e32 v68, v64, v68
	v_add_f32_e32 v68, v65, v68
	v_add_f32_e32 v68, v66, v68
	v_add_f32_e32 v68, v67, v68
	s_waitcnt lgkmcnt(0)
	v_mfma_f32_32x32x16_bf16 v[112:127], v[224:227], v[144:147], v[112:127]
	v_add_f32_e32 v68, v105, v68
	v_add_f32_e32 v68, v106, v68
	v_add_f32_e32 v68, v107, v68
	v_add_f32_e32 v68, v72, v68
	v_add_f32_e32 v68, v73, v68
	v_add_f32_e32 v211, v74, v68
	v_cvt_pk_bf16_f32 v108, v173, v175
	v_cvt_pk_bf16_f32 v109, v171, v174
	v_cvt_pk_bf16_f32 v110, v169, v172
	v_cvt_pk_bf16_f32 v111, v168, v170
	v_cvt_pk_bf16_f32 v100, v180, v182
	v_cvt_pk_bf16_f32 v101, v213, v214
	v_cvt_pk_bf16_f32 v102, v219, v228
	v_cvt_pk_bf16_f32 v103, v64, v65
	v_cvt_pk_bf16_f32 v104, v66, v67
	v_cvt_pk_bf16_f32 v105, v105, v106
	v_cvt_pk_bf16_f32 v106, v107, v72
	v_cvt_pk_bf16_f32 v107, v73, v74
	s_add_u32 s66, s46, s28
	s_addc_u32 s67, s47, s29
	s_add_u32 s34, s66, 0x23808000
	s_addc_u32 s35, s67, 0
	s_add_u32 s76, s66, 0x2380a000
	s_addc_u32 s77, s67, 0
	s_add_u32 s74, s46, s24
	s_addc_u32 s75, s47, s25
	s_add_u32 s78, s74, 0x21804000
	s_addc_u32 s79, s75, 0
	s_lshl_b32 s92, s57, 14
	s_add_i32 s92, s92, s94
	s_mov_b32 m0, s92
	s_lshl_b32 s96, s57, 13
	global_load_lds_dwordx4 v249, s[34:35]
	s_addk_i32 s92, 0x400
	s_mov_b32 m0, s92
	s_add_i32 s96, s96, s95
	global_load_lds_dwordx4 v250, s[34:35]
	s_nop 0
	s_mov_b32 m0, s96
	s_nop 0
	global_load_lds_dwordx4 v251, s[78:79]
	s_andn2_b64 vcc, exec, s[2:3]
	s_cbranch_vccnz .LBB4_851
	s_mov_b64 s[2:3], s[8:9]
	global_store_dwordx2 v188, v[184:185], s[2:3] nt

; #define AT_SBAR() __builtin_amdgcn_sched_barrier(0)
; template <int OFF> DI s16x4 tr_read(int vb) { s16x4 r; asm volatile("ds_read_b64_tr_b16 %0, %1 offset:%2" : "=&v"(r) : "v"(vb), "i"(OFF) : "memory"); return r; }
; template <int D0> DI void pv_one(f32x16& od, int vb, bf16x8 pa0, bf16x8 pa1, bf16x8 pa2, bf16x8 pa3) {
;     const s16x4 l0 = tr_read<v_rd_off(D0, 0, 0)>(vb), h0 = tr_read<v_rd_off(D0, 0, 1)>(vb), l1 = tr_read<v_rd_off(D0, 1, 0)>(vb), h1 = tr_read<v_rd_off(D0, 1, 1)>(vb);
;     const s16x4 l2 = tr_read<v_rd_off(D0, 2, 0)>(vb), h2 = tr_read<v_rd_off(D0, 2, 1)>(vb), l3 = tr_read<v_rd_off(D0, 3, 0)>(vb), h3 = tr_read<v_rd_off(D0, 3, 1)>(vb);
;     asm volatile("s_waitcnt lgkmcnt(0)" ::: "memory"); AT_SBAR();
;     ...
;     od = __builtin_amdgcn_mfma_f32_32x32x16_bf16(AT_PK(l0, h0), pa0, od, 0, 0, 0);
;     od = __builtin_amdgcn_mfma_f32_32x32x16_bf16(AT_PK(l1, h1), pa1, od, 0, 0, 0);
;     od = __builtin_amdgcn_mfma_f32_32x32x16_bf16(AT_PK(l2, h2), pa2, od, 0, 0, 0);
;     od = __builtin_amdgcn_mfma_f32_32x32x16_bf16(AT_PK(l3, h3), pa3, od, 0, 0, 0);
; DI void attn_pass(const Frame& F, CvRide& cv, const bf16_t* __restrict__ Qb, const bf16_t* __restrict__ Kh, const bf16_t* __restrict__ Vh, char* lds, f32x16 (&o)[4], float& l_out, const int wave_s) {
;     ...
;     const unsigned cv_ldo = (unsigned)(((tid >> 4) * 2 * 2048 + (tid & 15) * 4) * 4), cv_sto = (unsigned)((tid >> 3) * 2048 + 8 * (tid & 7));
;     const int cv_lw = OFF_CV + (4 * (tid & 15)) * 68 + 2 * (tid >> 4), cv_lr = OFF_CV + (tid >> 3) * 68 + 8 * (tid & 7);
;     f32x4 cvA = f32x4{}, cvB = f32x4{}; unsigned cvr0 = 0, cvr1 = 0;
.LBB4_853:
	ds_read_b64_tr_b16 v[214:215], v182 offset:0x600
	ds_read_b64_tr_b16 v[216:217], v182 offset:0x700
	ds_read_b64_tr_b16 v[218:219], v182 offset:0x1600
	ds_read_b64_tr_b16 v[220:221], v182 offset:0x1700
	ds_read_b64_tr_b16 v[222:223], v182 offset:0x2600
	ds_read_b64_tr_b16 v[224:225], v182 offset:0x2700
	ds_read_b64_tr_b16 v[226:227], v182 offset:0x3600
	ds_read_b64_tr_b16 v[228:229], v182 offset:0x3700
	s_waitcnt lgkmcnt(0)
	v_mfma_f32_32x32x16_bf16 v[0:15], v[214:217], v[96:99], v[0:15]
	s_lshl_b32 s2, s57, 14
	s_lshl_b32 s3, s57, 13
	s_sub_i32 s76, s2, s3
	s_waitcnt vmcnt(3)
	v_mfma_f32_32x32x16_bf16 v[0:15], v[218:221], v[108:111], v[0:15]
	s_andn2_b64 s[2:3], exec, s[30:31]
	s_andn2_b64 vcc, exec, s[30:31]
	v_mfma_f32_32x32x16_bf16 v[0:15], v[222:225], v[100:103], v[0:15]
	v_mfma_f32_32x32x16_bf16 v[0:15], v[226:229], v[104:107], v[0:15]
	s_cbranch_vccnz .LBB4_858
	v_med3_f32 v97, v160, -v255, v255
	v_med3_f32 v98, v164, -v255, v255
	v_cvt_scalef32_pk_fp8_f32 v99, v97, v98, s93
	v_med3_f32 v97, v161, -v255, v255
	v_med3_f32 v98, v165, -v255, v255
	v_cvt_scalef32_pk_fp8_f32 v100, v97, v98, s93
	v_med3_f32 v97, v162, -v255, v255
	v_med3_f32 v98, v166, -v255, v255
	s_bitcmp1_b32 s58, 0
	v_cvt_scalef32_pk_fp8_f32 v101, v97, v98, s93
	s_cselect_b32 s8, 0x1100, 0
	v_med3_f32 v97, v163, -v255, v255
	v_med3_f32 v98, v167, -v255, v255
	v_cmp_eq_u32_e32 vcc, 0, v181
	v_add_u32_e32 v96, s8, v190
	v_cvt_scalef32_pk_fp8_f32 v102, v97, v98, s93
	s_and_b64 vcc, exec, vcc
	s_and_b32 s30, s58, 31
	ds_write_b16 v96, v99
	ds_write_b16 v96, v100 offset:68
	ds_write_b16 v96, v101 offset:136
	ds_write_b16 v96, v102 offset:204
	s_cbranch_vccnz .LBB4_882
	s_lshl_b32 s8, s30, 7
	s_lshl_b32 s9, s58, 6
	s_and_b32 s8, s8, 0xf00
	s_and_b32 s9, s9, 64
	s_or_b32 s26, s8, s9
	s_cbranch_execnz .LBB4_857

.LBB4_860:
	s_and_b64 vcc, exec, s[2:3]
	s_waitcnt vmcnt(0) lgkmcnt(0)
	s_barrier
	v_add_u32_e32 v100, s76, v203
	ds_read_b128 v[96:99], v100 offset:49152
	ds_read_b128 v[168:171], v100 offset:53248
	s_cbranch_vccnz .LBB4_862
	s_andn2_b32 s26, 1, s58
	s_mulk_i32 s26, 0x1100
	v_add_u32_e32 v252, s26, v189
	ds_read2_b32 v[184:185], v252 offset1:1

; DI void finishSM(f32x16& p0, f32x16& p1, float alpha, float& l_reg, bf16x8& pa0, bf16x8& pa1, bf16x8& pa2, bf16x8& pa3) {
; #pragma unroll
;     for (int r = 0; r < 16; ++r) p1[r] = __builtin_amdgcn_exp2f(p1[r]);
;     float ps = 0;
; #pragma unroll
;     for (int r = 0; r < 16; ++r) ps += p0[r];
; #pragma unroll
;     for (int r = 0; r < 16; ++r) ps += p1[r];
;     { auto rr = __builtin_amdgcn_permlane32_swap(__float_as_uint(ps), __float_as_uint(ps), false, false); ps = __uint_as_float(rr[0]) + __uint_as_float(rr[1]); }
;     l_reg = l_reg * alpha + ps;
;     ...
;     AT_PK4(p0, 0, pa0); AT_PK4(p0, 8, pa1); AT_PK4(p1, 0, pa2); AT_PK4(p1, 8, pa3);
;     ...
; }
; DI void qkt(f32x16& p0, f32x16& p1, const char* Ks, const bf16x8* qr, const f32x16& negm, int r32, int hi) {
; #pragma unroll
;     for (int d0 = 0; d0 < 4; ++d0) { const int cb = (d0 * 16 + hi * 8) * 2;
;         const bf16x8 b0 = *reinterpret_cast<const bf16x8*>(Ks + AT_KSWZ(r32, cb));
;         const bf16x8 b1 = *reinterpret_cast<const bf16x8*>(Ks + AT_KSWZ(32 + r32, cb));
;         p0 = __builtin_amdgcn_mfma_f32_32x32x16_bf16(b0, qr[d0], d0 == 0 ? negm : p0, 0, 0, 0);
;         p1 = __builtin_amdgcn_mfma_f32_32x32x16_bf16(b1, qr[d0], d0 == 0 ? negm : p1, 0, 0, 0); }
; }
.LBB4_870:
	v_exp_f32_e32 v182, v128
	v_exp_f32_e32 v230, v129
	v_exp_f32_e32 v231, v130
	v_exp_f32_e32 v232, v131
	v_exp_f32_e32 v233, v132
	v_exp_f32_e32 v234, v133
	v_exp_f32_e32 v235, v134
	v_exp_f32_e32 v236, v135
	v_exp_f32_e32 v237, v136
	v_exp_f32_e32 v238, v137
	v_exp_f32_e32 v239, v138
	v_exp_f32_e32 v240, v139
	v_exp_f32_e32 v241, v140
	v_exp_f32_e32 v242, v141
	v_exp_f32_e32 v243, v142
	v_exp_f32_e32 v244, v143
	v_add_u32_e32 v101, s76, v204
	v_add_u32_e32 v102, s76, v205
	v_add_u32_e32 v103, s76, v206
	ds_read_b128 v[172:175], v101 offset:49152
	ds_read_b128 v[176:179], v101 offset:53248
	ds_read_b128 v[214:217], v102 offset:49152
	ds_read_b128 v[218:221], v102 offset:53248
	ds_read_b128 v[222:225], v103 offset:49152
	ds_read_b128 v[226:229], v103 offset:53248
	v_exp_f32_e32 v112, v112
	v_exp_f32_e32 v113, v113
	v_exp_f32_e32 v114, v114
	s_waitcnt lgkmcnt(7)
	v_mfma_f32_32x32x16_bf16 v[128:143], v[96:99], v[156:159], v[80:95]
	v_exp_f32_e32 v115, v115
	v_exp_f32_e32 v116, v116
	v_exp_f32_e32 v117, v117
	v_exp_f32_e32 v118, v118
	v_exp_f32_e32 v119, v119
	s_waitcnt lgkmcnt(6)
	v_mfma_f32_32x32x16_bf16 v[96:111], v[168:171], v[156:159], v[80:95]
	v_exp_f32_e32 v168, v120
	v_add_f32_e32 v120, 0, v182
	v_add_f32_e32 v120, v230, v120
	v_add_f32_e32 v120, v231, v120
	v_add_f32_e32 v120, v232, v120
	v_add_f32_e32 v120, v233, v120
	v_add_f32_e32 v120, v234, v120
	v_add_f32_e32 v120, v235, v120
	v_add_f32_e32 v120, v236, v120
	v_add_f32_e32 v120, v237, v120
	v_add_f32_e32 v120, v238, v120
	s_waitcnt lgkmcnt(5)
	v_mfma_f32_32x32x16_bf16 v[128:143], v[172:175], v[152:155], v[128:143]
	v_add_f32_e32 v120, v239, v120
	v_add_f32_e32 v120, v240, v120
	v_add_f32_e32 v120, v241, v120
	v_add_f32_e32 v120, v242, v120
	v_add_f32_e32 v120, v243, v120
	v_add_f32_e32 v120, v244, v120
	v_add_f32_e32 v120, v112, v120
	s_waitcnt lgkmcnt(4)
	v_mfma_f32_32x32x16_bf16 v[96:111], v[176:179], v[152:155], v[96:111]
	v_add_f32_e32 v120, v113, v120
	v_add_f32_e32 v120, v114, v120
	v_add_f32_e32 v120, v115, v120
	v_add_f32_e32 v120, v116, v120
	v_exp_f32_e32 v169, v121
	v_add_f32_e32 v120, v117, v120
	v_exp_f32_e32 v170, v122
	s_waitcnt lgkmcnt(3)
	v_mfma_f32_32x32x16_bf16 v[128:143], v[214:217], v[148:151], v[128:143]
	v_add_f32_e32 v120, v118, v120
	v_exp_f32_e32 v171, v123
	v_add_f32_e32 v120, v119, v120
	v_exp_f32_e32 v172, v124
	v_add_f32_e32 v120, v168, v120
	v_exp_f32_e32 v173, v125
	v_add_f32_e32 v120, v169, v120
	s_waitcnt lgkmcnt(2)
	v_mfma_f32_32x32x16_bf16 v[96:111], v[218:221], v[148:151], v[96:111]
	v_exp_f32_e32 v174, v126
	v_add_f32_e32 v120, v170, v120
	v_exp_f32_e32 v175, v127
	v_add_f32_e32 v120, v171, v120
	v_add_f32_e32 v120, v172, v120
	v_add_f32_e32 v120, v173, v120
	v_add_f32_e32 v120, v174, v120
	s_waitcnt lgkmcnt(1)
	v_mfma_f32_32x32x16_bf16 v[128:143], v[222:225], v[144:147], v[128:143]
	v_add_f32_e32 v213, v175, v120
	v_cvt_pk_bf16_f32 v120, v182, v230
	v_cvt_pk_bf16_f32 v121, v231, v232
	v_cvt_pk_bf16_f32 v122, v233, v234
	v_cvt_pk_bf16_f32 v123, v235, v236
	v_cvt_pk_bf16_f32 v124, v237, v238
	s_waitcnt lgkmcnt(0)
	v_mfma_f32_32x32x16_bf16 v[96:111], v[226:229], v[144:147], v[96:111]
	v_cvt_pk_bf16_f32 v125, v239, v240
	v_cvt_pk_bf16_f32 v126, v241, v242
	v_cvt_pk_bf16_f32 v127, v243, v244
	v_cvt_pk_bf16_f32 v112, v112, v113
	v_cvt_pk_bf16_f32 v113, v114, v115
	v_cvt_pk_bf16_f32 v114, v116, v117
	v_cvt_pk_bf16_f32 v115, v118, v119
	v_cvt_pk_bf16_f32 v116, v168, v169
	v_cvt_pk_bf16_f32 v117, v170, v171
	v_cvt_pk_bf16_f32 v118, v172, v173
	v_cvt_pk_bf16_f32 v119, v174, v175
	s_add_u32 s34, s66, 0x2380c000
	s_addc_u32 s35, s67, 0
	s_add_u32 s66, s66, 0x2380e000
	s_addc_u32 s67, s67, 0
	s_add_u32 s74, s74, 0x21806000
	s_addc_u32 s75, s75, 0
	s_lshl_b32 s92, s63, 14
	s_add_i32 s92, s92, s94
	s_mov_b32 m0, s92
	s_lshl_b32 s96, s63, 13
	global_load_lds_dwordx4 v249, s[34:35]
	s_addk_i32 s92, 0x400
	s_mov_b32 m0, s92
	s_add_i32 s96, s96, s95
	global_load_lds_dwordx4 v250, s[34:35]
	s_nop 0
	s_mov_b32 m0, s96
	s_nop 0
	global_load_lds_dwordx4 v251, s[74:75]
	s_nop 0
	s_and_b64 vcc, exec, s[2:3]
	s_cbranch_vccnz .LBB4_872
	s_mov_b64 s[2:3], s[8:9]
	global_store_dwordx2 v188, v[184:185], s[2:3] nt

; #define AT_SBAR() __builtin_amdgcn_sched_barrier(0)
; template <int OFF> DI s16x4 tr_read(int vb) { s16x4 r; asm volatile("ds_read_b64_tr_b16 %0, %1 offset:%2" : "=&v"(r) : "v"(vb), "i"(OFF) : "memory"); return r; }
; template <int D0> DI void pv_one(f32x16& od, int vb, bf16x8 pa0, bf16x8 pa1, bf16x8 pa2, bf16x8 pa3) {
;     const s16x4 l0 = tr_read<v_rd_off(D0, 0, 0)>(vb), h0 = tr_read<v_rd_off(D0, 0, 1)>(vb), l1 = tr_read<v_rd_off(D0, 1, 0)>(vb), h1 = tr_read<v_rd_off(D0, 1, 1)>(vb);
;     const s16x4 l2 = tr_read<v_rd_off(D0, 2, 0)>(vb), h2 = tr_read<v_rd_off(D0, 2, 1)>(vb), l3 = tr_read<v_rd_off(D0, 3, 0)>(vb), h3 = tr_read<v_rd_off(D0, 3, 1)>(vb);
;     asm volatile("s_waitcnt lgkmcnt(0)" ::: "memory"); AT_SBAR();
;     ...
;     od = __builtin_amdgcn_mfma_f32_32x32x16_bf16(AT_PK(l0, h0), pa0, od, 0, 0, 0);
;     od = __builtin_amdgcn_mfma_f32_32x32x16_bf16(AT_PK(l1, h1), pa1, od, 0, 0, 0);
;     od = __builtin_amdgcn_mfma_f32_32x32x16_bf16(AT_PK(l2, h2), pa2, od, 0, 0, 0);
;     od = __builtin_amdgcn_mfma_f32_32x32x16_bf16(AT_PK(l3, h3), pa3, od, 0, 0, 0);
; DI void attn_pass(const Frame& F, CvRide& cv, const bf16_t* __restrict__ Qb, const bf16_t* __restrict__ Kh, const bf16_t* __restrict__ Vh, char* lds, f32x16 (&o)[4], float& l_out, const int wave_s) {
;     ...
;     const unsigned cv_ldo = (unsigned)(((tid >> 4) * 2 * 2048 + (tid & 15) * 4) * 4), cv_sto = (unsigned)((tid >> 3) * 2048 + 8 * (tid & 7));
;     const int cv_lw = OFF_CV + (4 * (tid & 15)) * 68 + 2 * (tid >> 4), cv_lr = OFF_CV + (tid >> 3) * 68 + 8 * (tid & 7);
;     f32x4 cvA = f32x4{}, cvB = f32x4{}; unsigned cvr0 = 0, cvr1 = 0;
.LBB4_873:
	ds_read_b64_tr_b16 v[216:217], v215 offset:0x600
	ds_read_b64_tr_b16 v[218:219], v215 offset:0x700
	ds_read_b64_tr_b16 v[220:221], v215 offset:0x1600
	ds_read_b64_tr_b16 v[222:223], v215 offset:0x1700
	ds_read_b64_tr_b16 v[224:225], v215 offset:0x2600
	ds_read_b64_tr_b16 v[226:227], v215 offset:0x2700
	ds_read_b64_tr_b16 v[228:229], v215 offset:0x3600
	ds_read_b64_tr_b16 v[230:231], v215 offset:0x3700
	s_waitcnt lgkmcnt(0)
	v_mfma_f32_32x32x16_bf16 v[0:15], v[216:219], v[120:123], v[0:15]
	s_add_i32 s2, s65, 0
	s_waitcnt vmcnt(3)
	s_mov_b32 s26, 0
	s_andn2_b64 vcc, exec, s[30:31]
	v_mfma_f32_32x32x16_bf16 v[0:15], v[220:223], v[124:127], v[0:15]
	v_mfma_f32_32x32x16_bf16 v[0:15], v[224:227], v[112:115], v[0:15]
	s_andn2_b64 s[2:3], exec, s[30:31]
	v_mfma_f32_32x32x16_bf16 v[0:15], v[228:231], v[116:119], v[0:15]
	s_cbranch_vccnz .LBB4_878
	v_med3_f32 v113, v160, -v255, v255
	v_med3_f32 v114, v164, -v255, v255
	v_cvt_scalef32_pk_fp8_f32 v115, v113, v114, s93
	v_med3_f32 v113, v161, -v255, v255
	v_med3_f32 v114, v165, -v255, v255
	v_cvt_scalef32_pk_fp8_f32 v116, v113, v114, s93
	v_med3_f32 v113, v162, -v255, v255
	v_med3_f32 v114, v166, -v255, v255
	s_bitcmp1_b32 s58, 0
	v_cvt_scalef32_pk_fp8_f32 v117, v113, v114, s93
	s_cselect_b32 s8, 0x1100, 0
	v_med3_f32 v113, v163, -v255, v255
	v_med3_f32 v114, v167, -v255, v255
	v_cmp_eq_u32_e32 vcc, 0, v181
	v_add_u32_e32 v112, s8, v190
	v_cvt_scalef32_pk_fp8_f32 v118, v113, v114, s93
	s_and_b64 vcc, exec, vcc
	s_and_b32 s34, s58, 31
	ds_write_b16 v112, v115
	ds_write_b16 v112, v116 offset:68
	ds_write_b16 v112, v117 offset:136
	ds_write_b16 v112, v118 offset:204
	s_cbranch_vccnz .LBB4_883
	s_lshl_b32 s8, s34, 7
	s_lshl_b32 s9, s58, 6
	s_and_b32 s8, s8, 0xf00
	s_and_b32 s9, s9, 64
	s_or_b32 s26, s8, s9
	s_cbranch_execnz .LBB4_877

; DI void pv_all_sm(f32x16* o, int vb, bf16x8 pa0, bf16x8 pa1, bf16x8 pa2, bf16x8 pa3, f32x16& p0, f32x16& p1, float& m_ref, f32x16& negm, float& alpha) {
;     ...
; #pragma unroll
;     for (int r = 0; r < 16; ++r) p0[r] = __builtin_amdgcn_exp2f(p0[r]);
; DI void attn_pass(const Frame& F, CvRide& cv, const bf16_t* __restrict__ Qb, const bf16_t* __restrict__ Kh, const bf16_t* __restrict__ Vh, char* lds, f32x16 (&o)[4], float& l_out, const int wave_s) {
;     ...
;     for (int j = 1; j + 2 < NT; j += 2) {
;         AT_STEP(pB0, pB1, pA0, pA1, alB, alA, j, true);
;         AT_STEP(pA0, pA1, pB0, pB1, alA, alB, j + 1, true);
;     }
.LBB4_880:
	s_add_u32 s24, s24, 0x4000
	v_exp_f32_e32 v216, v128
	v_exp_f32_e32 v218, v129
	v_exp_f32_e32 v179, v130
	v_exp_f32_e32 v217, v131
	v_exp_f32_e32 v177, v132
	v_exp_f32_e32 v215, v133
	v_exp_f32_e32 v176, v134
	v_exp_f32_e32 v178, v135
	v_exp_f32_e32 v173, v136
	v_exp_f32_e32 v175, v137
	v_exp_f32_e32 v171, v138
	v_exp_f32_e32 v174, v139
	v_exp_f32_e32 v169, v140
	v_exp_f32_e32 v172, v141
	v_exp_f32_e32 v168, v142
	v_exp_f32_e32 v170, v143
	s_addc_u32 s25, s25, 0
	s_add_u32 s28, s28, 0x8000
	v_fma_f32 v112, v207, v183, v211
	s_addc_u32 s29, s29, 0
	s_add_i32 s23, s23, 2
	v_fma_f32 v183, v112, v180, v213
	s_cmp_gt_u32 s23, 61
	s_waitcnt vmcnt(0) lgkmcnt(0)
	s_barrier
	s_cbranch_scc1 .LBB4_886
	s_mov_b32 s30, s57
	s_mov_b32 s57, s64
	v_mov_b32_e32 v207, v182
	s_branch .LBB4_839

; DI int tid_fresh(int wave) { return wave * 64 + lane_fresh(); }
; DI void attn_pass(const Frame& F, CvRide& cv, const bf16_t* __restrict__ Qb, const bf16_t* __restrict__ Kh, const bf16_t* __restrict__ Vh, char* lds, f32x16 (&o)[4], float& l_out, const int wave_s) {
;     const int tid = tid_fresh(wave_s), wid = tid >> 6, lane = tid & 63, r32 = lane & 31, hi = lane >> 5;
;     char* V_lds = lds + OFF_V; char* K_lds = lds + OFF_K;
;     float m_ref = 0.f, l_reg = 0.f; bf16x8 qr[4]; f32x16 negm = f32x16{};
; #pragma unroll
;     for (int d = 0; d < 4; ++d) o[d] = f32x16{};
;     const bf16_t* Qw = Qb + (size_t)(wid * 32 + r32) * 64 + hi * 8;
; #pragma unroll
;     for (int d0 = 0; d0 < 4; ++d0) qr[d0] = *reinterpret_cast<const bf16x8*>(Qw + d0 * 16);
;     const int sr = tid >> 4, sc = (tid & 15) * 8, vst0 = v_st(sr, sc), vst1 = v_st(32 + sr, sc);
;     const int kr = tid >> 3, kcb = (tid & 7) * 16, kst = AT_KSWZ(kr, kcb);
;     const int vb0 = (int)(uintptr_t)V_lds + v_rd_base(lane);
;     struct { bf16x8 vs0, vs1, ks0; } sr_[1];
;     const unsigned gvo = (unsigned)((sr * 128 + sc) * 2), gko = (unsigned)((kr * 64 + (tid & 7) * 8) * 2);
;     ...
;     const unsigned cv_ldo = (unsigned)(((tid >> 4) * 2 * 2048 + (tid & 15) * 4) * 4), cv_sto = (unsigned)((tid >> 3) * 2048 + 8 * (tid & 7));
;     const int cv_lw = OFF_CV + (4 * (tid & 15)) * 68 + 2 * (tid >> 4), cv_lr = OFF_CV + (tid >> 3) * 68 + 8 * (tid & 7);
;     f32x4 cvA = f32x4{}, cvB = f32x4{}; unsigned cvr0 = 0, cvr1 = 0;
;     ...
;     f32x16 pA0, pA1, pB0, pB1; float alA, alB; bf16x8 pa0, pa1, pa2, pa3; constexpr int NT = S / 64;
;     constexpr int SE = 0;
;     {
;         bf16x8 v10 = *reinterpret_cast<const bf16x8*>(&Vh[(size_t)(64 + sr) * 128 + sc]), v11 = *reinterpret_cast<const bf16x8*>(&Vh[(size_t)(96 + sr) * 128 + sc]);
;         bf16x8 k10 = *reinterpret_cast<const bf16x8*>(&Kh[(size_t)(64 + kr) * 64 + (tid & 7) * 8]);
;         AT_SLOAD(SE, 0); asm volatile("s_waitcnt vmcnt(0)" ::: "memory");
;         __syncthreads();
;         AT_SWRITE(0, SE);
;         *(bf16x8*)(V_lds + SHM_V + vst0) = v10; *(bf16x8*)(V_lds + SHM_V + vst1) = v11; *(bf16x8*)(K_lds + SHM_K + kst) = k10;
;         __syncthreads();
;     }
;     qkt(pA0, pA1, K_lds, qr, negm, r32, hi); partialSM(pA0, pA1, m_ref, negm, alA);
;     int s_prev = 0, s_cur = 1, s_next = 2;
.LBB4_912:
	v_lshlrev_b32_e32 v24, 4, v22
	v_lshlrev_b32_e32 v23, 3, v22
	v_and_b32_e32 v24, 0xc0, v24
	v_lshlrev_b32_e32 v22, 1, v22
	v_and_or_b32 v24, v23, 24, v24
	v_and_b32_e32 v22, 32, v22
	v_and_b32_e32 v23, 0x100, v23
	s_cmp_lg_u32 0, -1
	v_or3_b32 v202, v24, v22, v23
	s_cselect_b32 s2, 0, 0
	v_add_u32_e32 v192, s2, v202
	s_movk_i32 s2, 0x44
	v_lshl_or_b32 v213, v16, 14, v18
	v_mul_lo_u32 v16, v20, s2
	v_exp_f32_e32 v220, v0
	v_add_u32_e32 v0, 0, v21
	s_mov_b32 s2, 0x22000
	v_add3_u32 v194, v0, v16, s2
	v_add_u32_e32 v0, 0, v19
	v_add3_u32 v195, v0, v17, s2
	s_and_b32 s2, s33, 7
	s_lshl_b32 s2, s2, 2
	s_lshl_b32 s3, s60, 1
	v_exp_f32_e32 v222, v1
	v_exp_f32_e32 v179, v2
	v_exp_f32_e32 v221, v3
	v_exp_f32_e32 v177, v4
	v_exp_f32_e32 v219, v5
	v_exp_f32_e32 v176, v6
	v_exp_f32_e32 v178, v7
	v_exp_f32_e32 v173, v8
	v_exp_f32_e32 v175, v9
	v_exp_f32_e32 v171, v10
	v_exp_f32_e32 v174, v11
	v_exp_f32_e32 v169, v12
	v_exp_f32_e32 v172, v13
	v_exp_f32_e32 v168, v14
	v_exp_f32_e32 v170, v15
	s_add_i32 s2, s2, s3
	s_add_i32 s2, s2, 32
	v_mov_b32_e32 v162, v183
	v_mov_b32_e32 v163, v183
	v_mov_b32_e32 v48, v183
	v_mov_b32_e32 v49, v183
	v_lshl_or_b32 v193, v20, 11, v21
	s_ashr_i32 s3, s2, 31
	v_mov_b32_e32 v182, v183
	v_mov_b32_e32 v160, v183
	v_mov_b32_e32 v161, v183
	v_mov_b32_e32 v50, v183
	v_mov_b32_e32 v51, v183
	v_mov_b32_e32 v52, v183
	v_mov_b32_e32 v53, v183
	v_mov_b32_e32 v54, v183
	v_mov_b32_e32 v55, v183
	v_mov_b32_e32 v56, v183
	v_mov_b32_e32 v57, v183
	v_mov_b32_e32 v58, v183
	v_mov_b32_e32 v59, v183
	v_mov_b32_e32 v60, v183
	v_mov_b32_e32 v61, v183
	v_mov_b32_e32 v62, v183
	v_mov_b32_e32 v63, v183
	v_mov_b64_e32 v[32:33], v[48:49]
	v_mov_b64_e32 v[16:17], v[48:49]
	v_mov_b64_e32 v[0:1], v[48:49]
	v_mov_b64_e32 v[166:167], v[162:163]
	s_mov_b32 s27, 1
	s_lshl_b64 s[20:21], s[2:3], 19
	s_mov_b32 s28, 0xc3e00000
	v_mov_b32_e32 v214, 0x43e00000
	s_mov_b32 s18, 0
	v_mov_b64_e32 v[34:35], v[50:51]
	v_mov_b64_e32 v[36:37], v[52:53]
	v_mov_b64_e32 v[38:39], v[54:55]
	v_mov_b64_e32 v[40:41], v[56:57]
	v_mov_b64_e32 v[42:43], v[58:59]
	v_mov_b64_e32 v[44:45], v[60:61]
	v_mov_b64_e32 v[46:47], v[62:63]
	v_mov_b64_e32 v[18:19], v[50:51]
	v_mov_b64_e32 v[20:21], v[52:53]
	v_mov_b64_e32 v[22:23], v[54:55]
	v_mov_b64_e32 v[24:25], v[56:57]
	v_mov_b64_e32 v[26:27], v[58:59]
	v_mov_b64_e32 v[28:29], v[60:61]
	v_mov_b64_e32 v[30:31], v[62:63]
	v_mov_b64_e32 v[2:3], v[50:51]
	v_mov_b64_e32 v[4:5], v[52:53]
	v_mov_b64_e32 v[6:7], v[54:55]
	v_mov_b64_e32 v[8:9], v[56:57]
	v_mov_b64_e32 v[10:11], v[58:59]
	v_mov_b64_e32 v[12:13], v[60:61]
	v_mov_b64_e32 v[14:15], v[62:63]
	v_mov_b64_e32 v[164:165], v[160:161]
	s_mov_b32 s22, 0
	s_mov_b32 s29, 1
	v_mov_b64_e32 v[184:185], v[182:183]
	v_mov_b32_e32 v81, v80
	v_mov_b32_e32 v82, v80
	v_mov_b32_e32 v83, v80
	v_mov_b32_e32 v84, v80
	v_mov_b32_e32 v85, v80
	v_mov_b32_e32 v86, v80
	v_mov_b32_e32 v87, v80
	v_mov_b32_e32 v88, v80
	v_mov_b32_e32 v89, v80
	v_mov_b32_e32 v90, v80
	v_mov_b32_e32 v91, v80
	v_mov_b32_e32 v92, v80
	v_mov_b32_e32 v93, v80
	v_mov_b32_e32 v94, v80
	v_mov_b32_e32 v95, v80
	v_mov_b32_e32 v255, 0x3f600000
	s_mov_b32 s93, 0x3b000000
	v_mbcnt_lo_u32_b32 v253, -1, 0
	v_mbcnt_hi_u32_b32 v253, -1, v253
	v_lshrrev_b32_e32 v253, 5, v253
	v_mul_u32_u24_e32 v253, 0x700, v253
	v_add_u32_e32 v253, v253, v192
	v_mbcnt_lo_u32_b32 v249, -1, 0
	v_mbcnt_hi_u32_b32 v249, -1, v249
	v_bfe_u32 v250, v249, 4, 1
	v_lshlrev_b32_e32 v250, 11, v250
	v_bfe_u32 v251, v249, 2, 2
	v_lshl_add_u32 v250, v251, 8, v250
	v_lshrrev_b32_e32 v251, 5, v249
	v_lshl_add_u32 v250, v251, 6, v250
	v_and_b32_e32 v251, 3, v249
	v_lshl_add_u32 v250, v251, 4, v250
	s_and_b32 s95, s69, 1
	s_lshr_b32 s94, s69, 1
	s_lshl_b32 s94, s94, 12
	s_lshl_b32 s96, s95, 10
	s_add_i32 s94, s94, s96
	v_lshrrev_b32_e32 v251, 4, v249
	v_lshl_add_u32 v251, s95, 2, v251
	v_and_b32_e32 v254, 7, v249
	v_xor_b32_e32 v251, v251, v254
	v_lshlrev_b32_e32 v251, 4, v251
	v_lshrrev_b32_e32 v254, 3, v249
	v_lshl_add_u32 v251, v254, 7, v251
	s_lshl_b32 s96, s69, 10
	v_add_u32_e32 v251, s96, v251
	v_add_u32_e32 v249, s94, v250
	v_add_u32_e32 v250, 0x80, v249
	s_lshl_b32 s94, s69, 11
	s_add_i32 s95, s96, 0xc000
	s_nop 0

; DI void finishSM(f32x16& p0, f32x16& p1, float alpha, float& l_reg, bf16x8& pa0, bf16x8& pa1, bf16x8& pa2, bf16x8& pa3) {
; #pragma unroll
;     for (int r = 0; r < 16; ++r) p1[r] = __builtin_amdgcn_exp2f(p1[r]);
;     float ps = 0;
; #pragma unroll
;     for (int r = 0; r < 16; ++r) ps += p0[r];
; #pragma unroll
;     for (int r = 0; r < 16; ++r) ps += p1[r];
;     { auto rr = __builtin_amdgcn_permlane32_swap(__float_as_uint(ps), __float_as_uint(ps), false, false); ps = __uint_as_float(rr[0]) + __uint_as_float(rr[1]); }
;     l_reg = l_reg * alpha + ps;
;     ...
;     AT_PK4(p0, 0, pa0); AT_PK4(p0, 8, pa1); AT_PK4(p1, 0, pa2); AT_PK4(p1, 8, pa3);
;     ...
; }
; DI void qkt(f32x16& p0, f32x16& p1, const char* Ks, const bf16x8* qr, const f32x16& negm, int r32, int hi) {
; #pragma unroll
;     for (int d0 = 0; d0 < 4; ++d0) { const int cb = (d0 * 16 + hi * 8) * 2;
;         const bf16x8 b0 = *reinterpret_cast<const bf16x8*>(Ks + AT_KSWZ(r32, cb));
;         const bf16x8 b1 = *reinterpret_cast<const bf16x8*>(Ks + AT_KSWZ(32 + r32, cb));
;         p0 = __builtin_amdgcn_mfma_f32_32x32x16_bf16(b0, qr[d0], d0 == 0 ? negm : p0, 0, 0, 0);
;         p1 = __builtin_amdgcn_mfma_f32_32x32x16_bf16(b1, qr[d0], d0 == 0 ? negm : p1, 0, 0, 0); }
; }
.LBB4_923:
	s_lshl_b32 s18, s30, 13
	s_add_i32 s18, s18, 0
	v_add_u32_e32 v72, s18, v208
	v_add_u32_e32 v112, s18, v209
	v_add_u32_e32 v180, s18, v210
	s_waitcnt lgkmcnt(1)
	v_mfma_f32_32x32x16_bf16 v[128:143], v[64:67], v[156:159], v[80:95]
	ds_read_b128 v[64:67], v72 offset:49152
	ds_read_b128 v[72:75], v72 offset:53248
	ds_read_b128 v[76:79], v112 offset:49152
	ds_read_b128 v[224:227], v112 offset:53248
	v_exp_f32_e32 v182, v97
	v_exp_f32_e32 v217, v98
	v_exp_f32_e32 v218, v99
	v_exp_f32_e32 v223, v100
	v_exp_f32_e32 v232, v101
	s_waitcnt lgkmcnt(4)
	v_mfma_f32_32x32x16_bf16 v[112:127], v[68:71], v[156:159], v[80:95]
	ds_read_b128 v[68:71], v180 offset:49152
	ds_read_b128 v[228:231], v180 offset:53248
	v_exp_f32_e32 v180, v96
	v_cvt_pk_bf16_f32 v96, v220, v222
	v_cvt_pk_bf16_f32 v97, v179, v221
	v_cvt_pk_bf16_f32 v98, v177, v219
	v_cvt_pk_bf16_f32 v99, v176, v178
	s_waitcnt lgkmcnt(4)
	v_mfma_f32_32x32x16_bf16 v[112:127], v[72:75], v[152:155], v[112:127]
	v_add_f32_e32 v75, 0, v220
	v_add_f32_e32 v75, v222, v75
	v_add_f32_e32 v75, v179, v75
	v_add_f32_e32 v75, v221, v75
	v_add_f32_e32 v75, v177, v75
	v_add_f32_e32 v75, v219, v75
	v_add_f32_e32 v75, v176, v75
	v_mfma_f32_32x32x16_bf16 v[128:143], v[64:67], v[152:155], v[128:143]
	v_add_f32_e32 v75, v178, v75
	v_add_f32_e32 v75, v173, v75
	v_add_f32_e32 v75, v175, v75
	v_add_f32_e32 v75, v171, v75
	v_add_f32_e32 v75, v174, v75
	v_add_f32_e32 v75, v169, v75
	v_add_f32_e32 v75, v172, v75
	s_waitcnt lgkmcnt(3)
	v_mfma_f32_32x32x16_bf16 v[128:143], v[76:79], v[148:151], v[128:143]
	v_add_f32_e32 v75, v168, v75
	v_add_f32_e32 v75, v170, v75
	v_add_f32_e32 v75, v180, v75
	v_add_f32_e32 v75, v182, v75
	v_exp_f32_e32 v64, v102
	v_exp_f32_e32 v65, v103
	v_exp_f32_e32 v66, v104
	s_waitcnt lgkmcnt(2)
	v_mfma_f32_32x32x16_bf16 v[112:127], v[224:227], v[148:151], v[112:127]
	v_exp_f32_e32 v67, v105
	v_exp_f32_e32 v105, v106
	v_exp_f32_e32 v106, v107
	v_exp_f32_e32 v107, v108
	v_exp_f32_e32 v72, v109
	v_exp_f32_e32 v73, v110
	v_exp_f32_e32 v74, v111
	s_waitcnt lgkmcnt(1)
	v_mfma_f32_32x32x16_bf16 v[128:143], v[68:71], v[144:147], v[128:143]
	v_add_f32_e32 v68, v217, v75
	v_add_f32_e32 v68, v218, v68
	v_add_f32_e32 v68, v223, v68
	v_add_f32_e32 v68, v232, v68
	v_add_f32_e32 v68, v64, v68
	v_add_f32_e32 v68, v65, v68
	v_add_f32_e32 v68, v66, v68
	v_add_f32_e32 v68, v67, v68
	s_waitcnt lgkmcnt(0)
	v_mfma_f32_32x32x16_bf16 v[112:127], v[228:231], v[144:147], v[112:127]
	v_add_f32_e32 v68, v105, v68
	v_add_f32_e32 v68, v106, v68
	v_add_f32_e32 v68, v107, v68
	v_add_f32_e32 v68, v72, v68
	v_add_f32_e32 v68, v73, v68
	v_add_f32_e32 v215, v74, v68
	v_cvt_pk_bf16_f32 v108, v173, v175
	v_cvt_pk_bf16_f32 v109, v171, v174
	v_cvt_pk_bf16_f32 v110, v169, v172
	v_cvt_pk_bf16_f32 v111, v168, v170
	v_cvt_pk_bf16_f32 v100, v180, v182
	v_cvt_pk_bf16_f32 v101, v217, v218
	v_cvt_pk_bf16_f32 v102, v223, v232
	v_cvt_pk_bf16_f32 v103, v64, v65
	v_cvt_pk_bf16_f32 v104, v66, v67
	v_cvt_pk_bf16_f32 v105, v105, v106
	v_cvt_pk_bf16_f32 v106, v107, v72
	v_cvt_pk_bf16_f32 v107, v73, v74
	s_add_u32 s34, s46, s16
	s_addc_u32 s35, s47, s17
	s_add_u32 s24, s34, 0x23808000
	s_addc_u32 s25, s35, 0
	s_add_u32 s54, s34, 0x2380a000
	s_addc_u32 s55, s35, 0
	s_add_u32 s42, s46, s20
	s_addc_u32 s43, s47, s21
	s_add_u32 s56, s42, 0x21884000
	s_addc_u32 s57, s43, 0
	s_lshl_b32 s92, s15, 14
	s_add_i32 s92, s92, s94
	s_mov_b32 m0, s92
	s_lshl_b32 s96, s15, 13
	global_load_lds_dwordx4 v249, s[24:25]
	s_addk_i32 s92, 0x400
	s_mov_b32 m0, s92
	s_add_i32 s96, s96, s95
	global_load_lds_dwordx4 v250, s[24:25]
	s_nop 0
	s_mov_b32 m0, s96
	s_nop 0
	global_load_lds_dwordx4 v251, s[56:57]
	s_andn2_b64 vcc, exec, s[2:3]
	s_cbranch_vccnz .LBB4_925
	s_mov_b64 s[2:3], s[8:9]
	global_store_dwordx2 v193, v[184:185], s[2:3] nt

; #define AT_SBAR() __builtin_amdgcn_sched_barrier(0)
; template <int OFF> DI s16x4 tr_read(int vb) { s16x4 r; asm volatile("ds_read_b64_tr_b16 %0, %1 offset:%2" : "=&v"(r) : "v"(vb), "i"(OFF) : "memory"); return r; }
; template <int D0> DI void pv_one(f32x16& od, int vb, bf16x8 pa0, bf16x8 pa1, bf16x8 pa2, bf16x8 pa3) {
;     const s16x4 l0 = tr_read<v_rd_off(D0, 0, 0)>(vb), h0 = tr_read<v_rd_off(D0, 0, 1)>(vb), l1 = tr_read<v_rd_off(D0, 1, 0)>(vb), h1 = tr_read<v_rd_off(D0, 1, 1)>(vb);
;     const s16x4 l2 = tr_read<v_rd_off(D0, 2, 0)>(vb), h2 = tr_read<v_rd_off(D0, 2, 1)>(vb), l3 = tr_read<v_rd_off(D0, 3, 0)>(vb), h3 = tr_read<v_rd_off(D0, 3, 1)>(vb);
;     asm volatile("s_waitcnt lgkmcnt(0)" ::: "memory"); AT_SBAR();
;     ...
;     od = __builtin_amdgcn_mfma_f32_32x32x16_bf16(AT_PK(l0, h0), pa0, od, 0, 0, 0);
;     od = __builtin_amdgcn_mfma_f32_32x32x16_bf16(AT_PK(l1, h1), pa1, od, 0, 0, 0);
;     od = __builtin_amdgcn_mfma_f32_32x32x16_bf16(AT_PK(l2, h2), pa2, od, 0, 0, 0);
;     od = __builtin_amdgcn_mfma_f32_32x32x16_bf16(AT_PK(l3, h3), pa3, od, 0, 0, 0);
; DI void attn_pass(const Frame& F, CvRide& cv, const bf16_t* __restrict__ Qb, const bf16_t* __restrict__ Kh, const bf16_t* __restrict__ Vh, char* lds, f32x16 (&o)[4], float& l_out, const int wave_s) {
;     ...
;     const unsigned cv_ldo = (unsigned)(((tid >> 4) * 2 * 2048 + (tid & 15) * 4) * 4), cv_sto = (unsigned)((tid >> 3) * 2048 + 8 * (tid & 7));
;     const int cv_lw = OFF_CV + (4 * (tid & 15)) * 68 + 2 * (tid >> 4), cv_lr = OFF_CV + (tid >> 3) * 68 + 8 * (tid & 7);
;     f32x4 cvA = f32x4{}, cvB = f32x4{}; unsigned cvr0 = 0, cvr1 = 0;
.LBB4_927:
	ds_read_b64_tr_b16 v[218:219], v182 offset:0x600
	ds_read_b64_tr_b16 v[220:221], v182 offset:0x700
	ds_read_b64_tr_b16 v[222:223], v182 offset:0x1600
	ds_read_b64_tr_b16 v[224:225], v182 offset:0x1700
	ds_read_b64_tr_b16 v[226:227], v182 offset:0x2600
	ds_read_b64_tr_b16 v[228:229], v182 offset:0x2700
	ds_read_b64_tr_b16 v[230:231], v182 offset:0x3600
	ds_read_b64_tr_b16 v[232:233], v182 offset:0x3700
	s_waitcnt lgkmcnt(0)
	v_mfma_f32_32x32x16_bf16 v[0:15], v[218:221], v[96:99], v[0:15]
	s_lshl_b32 s2, s15, 14
	s_lshl_b32 s3, s15, 13
	s_sub_i32 s54, s2, s3
	s_waitcnt vmcnt(3)
	v_mfma_f32_32x32x16_bf16 v[0:15], v[222:225], v[108:111], v[0:15]
	s_andn2_b64 s[2:3], exec, s[22:23]
	s_andn2_b64 vcc, exec, s[22:23]
	v_mfma_f32_32x32x16_bf16 v[0:15], v[226:229], v[100:103], v[0:15]
	v_mfma_f32_32x32x16_bf16 v[0:15], v[230:233], v[104:107], v[0:15]
	s_cbranch_vccnz .LBB4_932
	v_med3_f32 v97, v160, -v255, v255
	v_med3_f32 v98, v164, -v255, v255
	v_cvt_scalef32_pk_fp8_f32 v99, v97, v98, s93
	v_med3_f32 v97, v161, -v255, v255
	v_med3_f32 v98, v165, -v255, v255
	v_cvt_scalef32_pk_fp8_f32 v100, v97, v98, s93
	v_med3_f32 v97, v162, -v255, v255
	v_med3_f32 v98, v166, -v255, v255
	s_bitcmp1_b32 s58, 0
	v_cvt_scalef32_pk_fp8_f32 v101, v97, v98, s93
	s_cselect_b32 s8, 0x1100, 0
	v_med3_f32 v97, v163, -v255, v255
	v_med3_f32 v98, v167, -v255, v255
	v_cmp_eq_u32_e32 vcc, 0, v181
	v_add_u32_e32 v96, s8, v195
	v_cvt_scalef32_pk_fp8_f32 v102, v97, v98, s93
	s_and_b64 vcc, exec, vcc
	s_and_b32 s22, s58, 31
	ds_write_b16 v96, v99
	ds_write_b16 v96, v100 offset:68
	ds_write_b16 v96, v101 offset:136
	ds_write_b16 v96, v102 offset:204
	s_cbranch_vccnz .LBB4_956
	s_lshl_b32 s8, s22, 7
	s_lshl_b32 s9, s58, 6
	s_and_b32 s8, s8, 0xf00
	s_and_b32 s9, s9, 64
	s_or_b32 s18, s8, s9
	s_cbranch_execnz .LBB4_931

.LBB4_934:
	s_and_b64 vcc, exec, s[2:3]
	s_waitcnt vmcnt(0) lgkmcnt(0)
	s_barrier
	v_add_u32_e32 v100, s54, v207
	ds_read_b128 v[96:99], v100 offset:49152
	ds_read_b128 v[168:171], v100 offset:53248
	s_cbranch_vccnz .LBB4_936
	s_andn2_b32 s18, 1, s58
	s_mulk_i32 s18, 0x1100
	v_add_u32_e32 v252, s18, v194
	ds_read2_b32 v[184:185], v252 offset1:1

; DI void finishSM(f32x16& p0, f32x16& p1, float alpha, float& l_reg, bf16x8& pa0, bf16x8& pa1, bf16x8& pa2, bf16x8& pa3) {
; #pragma unroll
;     for (int r = 0; r < 16; ++r) p1[r] = __builtin_amdgcn_exp2f(p1[r]);
;     float ps = 0;
; #pragma unroll
;     for (int r = 0; r < 16; ++r) ps += p0[r];
; #pragma unroll
;     for (int r = 0; r < 16; ++r) ps += p1[r];
;     { auto rr = __builtin_amdgcn_permlane32_swap(__float_as_uint(ps), __float_as_uint(ps), false, false); ps = __uint_as_float(rr[0]) + __uint_as_float(rr[1]); }
;     l_reg = l_reg * alpha + ps;
;     ...
;     AT_PK4(p0, 0, pa0); AT_PK4(p0, 8, pa1); AT_PK4(p1, 0, pa2); AT_PK4(p1, 8, pa3);
;     ...
; }
; DI void qkt(f32x16& p0, f32x16& p1, const char* Ks, const bf16x8* qr, const f32x16& negm, int r32, int hi) {
; #pragma unroll
;     for (int d0 = 0; d0 < 4; ++d0) { const int cb = (d0 * 16 + hi * 8) * 2;
;         const bf16x8 b0 = *reinterpret_cast<const bf16x8*>(Ks + AT_KSWZ(r32, cb));
;         const bf16x8 b1 = *reinterpret_cast<const bf16x8*>(Ks + AT_KSWZ(32 + r32, cb));
;         p0 = __builtin_amdgcn_mfma_f32_32x32x16_bf16(b0, qr[d0], d0 == 0 ? negm : p0, 0, 0, 0);
;         p1 = __builtin_amdgcn_mfma_f32_32x32x16_bf16(b1, qr[d0], d0 == 0 ? negm : p1, 0, 0, 0); }
; }
.LBB4_944:
	v_exp_f32_e32 v182, v128
	v_exp_f32_e32 v234, v129
	v_exp_f32_e32 v235, v130
	v_exp_f32_e32 v236, v131
	v_exp_f32_e32 v237, v132
	v_exp_f32_e32 v238, v133
	v_exp_f32_e32 v239, v134
	v_exp_f32_e32 v240, v135
	v_exp_f32_e32 v241, v136
	v_exp_f32_e32 v242, v137
	v_exp_f32_e32 v243, v138
	v_exp_f32_e32 v244, v139
	v_exp_f32_e32 v245, v140
	v_exp_f32_e32 v246, v141
	v_exp_f32_e32 v247, v142
	v_exp_f32_e32 v248, v143
	v_add_u32_e32 v101, s54, v208
	v_add_u32_e32 v102, s54, v209
	v_add_u32_e32 v103, s54, v210
	ds_read_b128 v[172:175], v101 offset:49152
	ds_read_b128 v[176:179], v101 offset:53248
	ds_read_b128 v[218:221], v102 offset:49152
	ds_read_b128 v[222:225], v102 offset:53248
	ds_read_b128 v[226:229], v103 offset:49152
	ds_read_b128 v[230:233], v103 offset:53248
	v_exp_f32_e32 v112, v112
	v_exp_f32_e32 v113, v113
	v_exp_f32_e32 v114, v114
	s_waitcnt lgkmcnt(7)
	v_mfma_f32_32x32x16_bf16 v[128:143], v[96:99], v[156:159], v[80:95]
	v_exp_f32_e32 v115, v115
	v_exp_f32_e32 v116, v116
	v_exp_f32_e32 v117, v117
	v_exp_f32_e32 v118, v118
	v_exp_f32_e32 v119, v119
	s_waitcnt lgkmcnt(6)
	v_mfma_f32_32x32x16_bf16 v[96:111], v[168:171], v[156:159], v[80:95]
	v_exp_f32_e32 v168, v120
	v_add_f32_e32 v120, 0, v182
	v_add_f32_e32 v120, v234, v120
	v_add_f32_e32 v120, v235, v120
	v_add_f32_e32 v120, v236, v120
	v_add_f32_e32 v120, v237, v120
	v_add_f32_e32 v120, v238, v120
	v_add_f32_e32 v120, v239, v120
	v_add_f32_e32 v120, v240, v120
	v_add_f32_e32 v120, v241, v120
	v_add_f32_e32 v120, v242, v120
	s_waitcnt lgkmcnt(5)
	v_mfma_f32_32x32x16_bf16 v[128:143], v[172:175], v[152:155], v[128:143]
	v_add_f32_e32 v120, v243, v120
	v_add_f32_e32 v120, v244, v120
	v_add_f32_e32 v120, v245, v120
	v_add_f32_e32 v120, v246, v120
	v_add_f32_e32 v120, v247, v120
	v_add_f32_e32 v120, v248, v120
	v_add_f32_e32 v120, v112, v120
	s_waitcnt lgkmcnt(4)
	v_mfma_f32_32x32x16_bf16 v[96:111], v[176:179], v[152:155], v[96:111]
	v_add_f32_e32 v120, v113, v120
	v_add_f32_e32 v120, v114, v120
	v_add_f32_e32 v120, v115, v120
	v_add_f32_e32 v120, v116, v120
	v_exp_f32_e32 v169, v121
	v_add_f32_e32 v120, v117, v120
	v_exp_f32_e32 v170, v122
	s_waitcnt lgkmcnt(3)
	v_mfma_f32_32x32x16_bf16 v[128:143], v[218:221], v[148:151], v[128:143]
	v_add_f32_e32 v120, v118, v120
	v_exp_f32_e32 v171, v123
	v_add_f32_e32 v120, v119, v120
	v_exp_f32_e32 v172, v124
	v_add_f32_e32 v120, v168, v120
	v_exp_f32_e32 v173, v125
	v_add_f32_e32 v120, v169, v120
	s_waitcnt lgkmcnt(2)
	v_mfma_f32_32x32x16_bf16 v[96:111], v[222:225], v[148:151], v[96:111]
	v_exp_f32_e32 v174, v126
	v_add_f32_e32 v120, v170, v120
	v_exp_f32_e32 v175, v127
	v_add_f32_e32 v120, v171, v120
	v_add_f32_e32 v120, v172, v120
	v_add_f32_e32 v120, v173, v120
	v_add_f32_e32 v120, v174, v120
	s_waitcnt lgkmcnt(1)
	v_mfma_f32_32x32x16_bf16 v[128:143], v[226:229], v[144:147], v[128:143]
	v_add_f32_e32 v217, v175, v120
	v_cvt_pk_bf16_f32 v120, v182, v234
	v_cvt_pk_bf16_f32 v121, v235, v236
	v_cvt_pk_bf16_f32 v122, v237, v238
	v_cvt_pk_bf16_f32 v123, v239, v240
	v_cvt_pk_bf16_f32 v124, v241, v242
	s_waitcnt lgkmcnt(0)
	v_mfma_f32_32x32x16_bf16 v[96:111], v[230:233], v[144:147], v[96:111]
	v_cvt_pk_bf16_f32 v125, v243, v244
	v_cvt_pk_bf16_f32 v126, v245, v246
	v_cvt_pk_bf16_f32 v127, v247, v248
	v_cvt_pk_bf16_f32 v112, v112, v113
	v_cvt_pk_bf16_f32 v113, v114, v115
	v_cvt_pk_bf16_f32 v114, v116, v117
	v_cvt_pk_bf16_f32 v115, v118, v119
	v_cvt_pk_bf16_f32 v116, v168, v169
	v_cvt_pk_bf16_f32 v117, v170, v171
	v_cvt_pk_bf16_f32 v118, v172, v173
	v_cvt_pk_bf16_f32 v119, v174, v175
	s_add_u32 s24, s34, 0x2380c000
	s_addc_u32 s25, s35, 0
	s_add_u32 s34, s34, 0x2380e000
	s_addc_u32 s35, s35, 0
	s_add_u32 s42, s42, 0x21886000
	s_addc_u32 s43, s43, 0
	s_lshl_b32 s92, s29, 14
	s_add_i32 s92, s92, s94
	s_mov_b32 m0, s92
	s_lshl_b32 s96, s29, 13
	global_load_lds_dwordx4 v249, s[24:25]
	s_addk_i32 s92, 0x400
	s_mov_b32 m0, s92
	s_add_i32 s96, s96, s95
	global_load_lds_dwordx4 v250, s[24:25]
	s_nop 0
	s_mov_b32 m0, s96
	s_nop 0
	global_load_lds_dwordx4 v251, s[42:43]
	s_nop 0
	s_and_b64 vcc, exec, s[2:3]
	s_cbranch_vccnz .LBB4_946
	s_mov_b64 s[2:3], s[8:9]
	global_store_dwordx2 v193, v[184:185], s[2:3] nt

; #define AT_SBAR() __builtin_amdgcn_sched_barrier(0)
; template <int OFF> DI s16x4 tr_read(int vb) { s16x4 r; asm volatile("ds_read_b64_tr_b16 %0, %1 offset:%2" : "=&v"(r) : "v"(vb), "i"(OFF) : "memory"); return r; }
; template <int D0> DI void pv_one(f32x16& od, int vb, bf16x8 pa0, bf16x8 pa1, bf16x8 pa2, bf16x8 pa3) {
;     const s16x4 l0 = tr_read<v_rd_off(D0, 0, 0)>(vb), h0 = tr_read<v_rd_off(D0, 0, 1)>(vb), l1 = tr_read<v_rd_off(D0, 1, 0)>(vb), h1 = tr_read<v_rd_off(D0, 1, 1)>(vb);
;     const s16x4 l2 = tr_read<v_rd_off(D0, 2, 0)>(vb), h2 = tr_read<v_rd_off(D0, 2, 1)>(vb), l3 = tr_read<v_rd_off(D0, 3, 0)>(vb), h3 = tr_read<v_rd_off(D0, 3, 1)>(vb);
;     asm volatile("s_waitcnt lgkmcnt(0)" ::: "memory"); AT_SBAR();
;     ...
;     od = __builtin_amdgcn_mfma_f32_32x32x16_bf16(AT_PK(l0, h0), pa0, od, 0, 0, 0);
;     od = __builtin_amdgcn_mfma_f32_32x32x16_bf16(AT_PK(l1, h1), pa1, od, 0, 0, 0);
;     od = __builtin_amdgcn_mfma_f32_32x32x16_bf16(AT_PK(l2, h2), pa2, od, 0, 0, 0);
;     od = __builtin_amdgcn_mfma_f32_32x32x16_bf16(AT_PK(l3, h3), pa3, od, 0, 0, 0);
; DI void attn_pass(const Frame& F, CvRide& cv, const bf16_t* __restrict__ Qb, const bf16_t* __restrict__ Kh, const bf16_t* __restrict__ Vh, char* lds, f32x16 (&o)[4], float& l_out, const int wave_s) {
;     ...
;     const unsigned cv_ldo = (unsigned)(((tid >> 4) * 2 * 2048 + (tid & 15) * 4) * 4), cv_sto = (unsigned)((tid >> 3) * 2048 + 8 * (tid & 7));
;     const int cv_lw = OFF_CV + (4 * (tid & 15)) * 68 + 2 * (tid >> 4), cv_lr = OFF_CV + (tid >> 3) * 68 + 8 * (tid & 7);
;     f32x4 cvA = f32x4{}, cvB = f32x4{}; unsigned cvr0 = 0, cvr1 = 0;
.LBB4_947:
	ds_read_b64_tr_b16 v[220:221], v219 offset:0x600
	ds_read_b64_tr_b16 v[222:223], v219 offset:0x700
	ds_read_b64_tr_b16 v[224:225], v219 offset:0x1600
	ds_read_b64_tr_b16 v[226:227], v219 offset:0x1700
	ds_read_b64_tr_b16 v[228:229], v219 offset:0x2600
	ds_read_b64_tr_b16 v[230:231], v219 offset:0x2700
	ds_read_b64_tr_b16 v[232:233], v219 offset:0x3600
	ds_read_b64_tr_b16 v[234:235], v219 offset:0x3700
	s_waitcnt lgkmcnt(0)
	v_mfma_f32_32x32x16_bf16 v[0:15], v[220:223], v[120:123], v[0:15]
	s_add_i32 s2, s31, 0
	s_waitcnt vmcnt(3)
	s_mov_b32 s18, 0
	s_andn2_b64 vcc, exec, s[22:23]
	v_mfma_f32_32x32x16_bf16 v[0:15], v[224:227], v[124:127], v[0:15]
	v_mfma_f32_32x32x16_bf16 v[0:15], v[228:231], v[112:115], v[0:15]
	s_andn2_b64 s[2:3], exec, s[22:23]
	v_mfma_f32_32x32x16_bf16 v[0:15], v[232:235], v[116:119], v[0:15]
	s_cbranch_vccnz .LBB4_952
	v_med3_f32 v113, v160, -v255, v255
	v_med3_f32 v114, v164, -v255, v255
	v_cvt_scalef32_pk_fp8_f32 v115, v113, v114, s93
	v_med3_f32 v113, v161, -v255, v255
	v_med3_f32 v114, v165, -v255, v255
	v_cvt_scalef32_pk_fp8_f32 v116, v113, v114, s93
	v_med3_f32 v113, v162, -v255, v255
	v_med3_f32 v114, v166, -v255, v255
	s_bitcmp1_b32 s58, 0
	v_cvt_scalef32_pk_fp8_f32 v117, v113, v114, s93
	s_cselect_b32 s8, 0x1100, 0
	v_med3_f32 v113, v163, -v255, v255
	v_med3_f32 v114, v167, -v255, v255
	v_cmp_eq_u32_e32 vcc, 0, v181
	v_add_u32_e32 v112, s8, v195
	v_cvt_scalef32_pk_fp8_f32 v118, v113, v114, s93
	s_and_b64 vcc, exec, vcc
	s_and_b32 s24, s58, 31
	ds_write_b16 v112, v115
	ds_write_b16 v112, v116 offset:68
	ds_write_b16 v112, v117 offset:136
	ds_write_b16 v112, v118 offset:204
	s_cbranch_vccnz .LBB4_957
	s_lshl_b32 s8, s24, 7
	s_lshl_b32 s9, s58, 6
	s_and_b32 s8, s8, 0xf00
	s_and_b32 s9, s9, 64
	s_or_b32 s18, s8, s9
	s_cbranch_execnz .LBB4_951

; DI void pv_all_sm(f32x16* o, int vb, bf16x8 pa0, bf16x8 pa1, bf16x8 pa2, bf16x8 pa3, f32x16& p0, f32x16& p1, float& m_ref, f32x16& negm, float& alpha) {
;     ...
; #pragma unroll
;     for (int r = 0; r < 16; ++r) p0[r] = __builtin_amdgcn_exp2f(p0[r]);
; DI void attn_pass(const Frame& F, CvRide& cv, const bf16_t* __restrict__ Qb, const bf16_t* __restrict__ Kh, const bf16_t* __restrict__ Vh, char* lds, f32x16 (&o)[4], float& l_out, const int wave_s) {
;     ...
;     for (int j = 1; j + 2 < NT; j += 2) {
;         AT_STEP(pB0, pB1, pA0, pA1, alB, alA, j, true);
;         AT_STEP(pA0, pA1, pB0, pB1, alA, alB, j + 1, true);
;     }
.LBB4_954:
	s_add_u32 s20, s20, 0x4000
	v_exp_f32_e32 v220, v128
	v_exp_f32_e32 v222, v129
	v_exp_f32_e32 v179, v130
	v_exp_f32_e32 v221, v131
	v_exp_f32_e32 v177, v132
	v_exp_f32_e32 v219, v133
	v_exp_f32_e32 v176, v134
	v_exp_f32_e32 v178, v135
	v_exp_f32_e32 v173, v136
	v_exp_f32_e32 v175, v137
	v_exp_f32_e32 v171, v138
	v_exp_f32_e32 v174, v139
	v_exp_f32_e32 v169, v140
	v_exp_f32_e32 v172, v141
	v_exp_f32_e32 v168, v142
	v_exp_f32_e32 v170, v143
	s_addc_u32 s21, s21, 0
	s_add_u32 s16, s16, 0x8000
	v_fma_f32 v112, v211, v183, v215
	s_addc_u32 s17, s17, 0
	s_add_i32 s27, s27, 2
	v_fma_f32 v183, v112, v180, v217
	s_cmp_gt_u32 s27, 61
	s_waitcnt vmcnt(0) lgkmcnt(0)
	s_barrier
	s_cbranch_scc1 .LBB4_960
	s_mov_b32 s22, s15
	s_mov_b32 s15, s30
	v_mov_b32_e32 v211, v182
	s_branch .LBB4_913

; #define LAS __attribute__((address_space(3)))
; __global__ void __launch_bounds__(NTHR, 2) mega(Args a) {
;     extern __shared__ __attribute__((aligned(16))) unsigned char lds[];
;     Frame F;
;     F.lds = lds; F.ldsl = (LAS unsigned char*)lds; F.ws = a.ws; F.in = a.in; F.out = a.out;
;     F.wg = blockIdx.x; F.nwg = gridDim.x;
;     F.wave = __builtin_amdgcn_readfirstlane(threadIdx.x >> 6);
	.amdhsa_kernel _Z4mega4Args
		.amdhsa_group_segment_fixed_size 0
		.amdhsa_private_segment_fixed_size 0
		.amdhsa_kernarg_size 456
		.amdhsa_user_sgpr_count 2
		.amdhsa_user_sgpr_dispatch_ptr 0
		.amdhsa_user_sgpr_queue_ptr 0
		.amdhsa_user_sgpr_kernarg_segment_ptr 1
		.amdhsa_user_sgpr_dispatch_id 0
		.amdhsa_user_sgpr_kernarg_preload_length 0
		.amdhsa_user_sgpr_kernarg_preload_offset 0
		.amdhsa_user_sgpr_private_segment_size 0
		.amdhsa_uses_dynamic_stack 0
		.amdhsa_enable_private_segment 0
		.amdhsa_system_sgpr_workgroup_id_x 1
		.amdhsa_system_sgpr_workgroup_id_y 0
		.amdhsa_system_sgpr_workgroup_id_z 0
		.amdhsa_system_sgpr_workgroup_info 0
		.amdhsa_system_vgpr_workitem_id 0
		.amdhsa_next_free_vgpr 256
		.amdhsa_next_free_sgpr 102
		.amdhsa_accum_offset 256
		.amdhsa_reserve_vcc 1
		.amdhsa_float_round_mode_32 0
		.amdhsa_float_round_mode_16_64 0
		.amdhsa_float_denorm_mode_32 3
		.amdhsa_float_denorm_mode_16_64 3
		.amdhsa_dx10_clamp 1
		.amdhsa_ieee_mode 1
		.amdhsa_fp16_overflow 0
		.amdhsa_tg_split 0
		.amdhsa_exception_fp_ieee_invalid_op 0
		.amdhsa_exception_fp_denorm_src 0
		.amdhsa_exception_fp_ieee_div_zero 0
		.amdhsa_exception_fp_ieee_overflow 0
		.amdhsa_exception_fp_ieee_underflow 0
		.amdhsa_exception_fp_ieee_inexact 0
		.amdhsa_exception_int_div_zero 0
	.end_amdhsa_kernel

; __global__ void __launch_bounds__(256) k_attn_naive(const bf16_t* __restrict__ QD, const bf16_t* __restrict__ KD, const bf16_t* __restrict__ VD, float* __restrict__ On) {
;     __shared__ __attribute__((aligned(16))) bf16_t Ks[32][64];
;     __shared__ __attribute__((aligned(16))) bf16_t Vs[32][128];
;     const int t = threadIdx.x, bid = blockIdx.x, qb = bid & 15, bhm = bid >> 4, bh = bhm >> 1;
; __global__ void __launch_bounds__(256) k_ret_naive(const bf16_t* __restrict__ RQ, const bf16_t* __restrict__ RK, const bf16_t* __restrict__ RV, const float* __restrict__ logit, float* __restrict__ Oraw) {
;     __shared__ __attribute__((aligned(16))) bf16_t Ks[32][128];
;     __shared__ __attribute__((aligned(16))) bf16_t Vs[32][64];
;     const int t = threadIdx.x, bid = blockIdx.x, sb = bid & 15, hf = (bid >> 4) & 1, bh = bid >> 5, h = bh & 7;
;     const int s = sb * 256 + t;
;     const float gf = 1.f / (1.f + __expf(-logit[h])), gb = 1.f / (1.f + __expf(-logit[8 + h]));
;     const float lgf = log2f(gf), lgb = log2f(gb);
amdhsa.kernels:
  - .agpr_count:     0
    .args:
      - .actual_access:  read_only
        .address_space:  global
        .offset:         0
        .size:           8
        .value_kind:     global_buffer
      - .actual_access:  read_only
        .address_space:  global
        .offset:         8
        .size:           8
        .value_kind:     global_buffer
      - .actual_access:  read_only
        .address_space:  global
        .offset:         16
        .size:           8
        .value_kind:     global_buffer
      - .actual_access:  write_only
        .address_space:  global
        .offset:         24
        .size:           8
        .value_kind:     global_buffer
    .group_segment_fixed_size: 12288
    .kernarg_segment_align: 8
    .kernarg_segment_size: 32
    .language:       OpenCL C
    .language_version:
      - 2
      - 0
    .max_flat_workgroup_size: 256
    .name:           _Z12k_attn_naivePKtS0_S0_Pf
    .private_segment_fixed_size: 0
    .sgpr_count:     18
    .sgpr_spill_count: 0
    .symbol:         _Z12k_attn_naivePKtS0_S0_Pf.kd
    .uniform_work_group_size: 1
    .uses_dynamic_stack: false
    .vgpr_count:     232
    .vgpr_spill_count: 0
    .wavefront_size: 64
  - .agpr_count:     0
    .args:
      - .actual_access:  read_only
        .address_space:  global
        .offset:         0
        .size:           8
        .value_kind:     global_buffer
      - .address_space:  global
        .offset:         8
        .size:           8
        .value_kind:     global_buffer
      - .address_space:  global
        .offset:         16
        .size:           8
        .value_kind:     global_buffer
      - .address_space:  global
        .offset:         24
        .size:           8
        .value_kind:     global_buffer
      - .address_space:  global
        .offset:         32
        .size:           8
        .value_kind:     global_buffer
      - .actual_access:  read_only
        .address_space:  global
        .offset:         40
        .size:           8
        .value_kind:     global_buffer
      - .actual_access:  write_only
        .address_space:  global
        .offset:         48
        .size:           8
        .value_kind:     global_buffer
    .group_segment_fixed_size: 0
    .kernarg_segment_align: 8
    .kernarg_segment_size: 56
    .language:       OpenCL C
    .language_version:
      - 2
      - 0
    .max_flat_workgroup_size: 256
    .name:           _Z14k_attn_combinePKfS0_S0_S0_S0_S0_Pt
    .private_segment_fixed_size: 0
    .sgpr_count:     18
    .sgpr_spill_count: 0
    .symbol:         _Z14k_attn_combinePKfS0_S0_S0_S0_S0_Pt.kd
    .uniform_work_group_size: 1
    .uses_dynamic_stack: false
    .vgpr_count:     19
    .vgpr_spill_count: 0
    .wavefront_size: 64
  - .agpr_count:     0
    .args:
      - .actual_access:  read_only
        .address_space:  global
        .offset:         0
        .size:           8
        .value_kind:     global_buffer
      - .actual_access:  read_only
        .address_space:  global
        .offset:         8
        .size:           8
        .value_kind:     global_buffer
      - .actual_access:  read_only
        .address_space:  global
        .offset:         16
        .size:           8
        .value_kind:     global_buffer
      - .actual_access:  read_only
        .address_space:  global
        .offset:         24
        .size:           8
        .value_kind:     global_buffer
      - .actual_access:  write_only
        .address_space:  global
        .offset:         32
        .size:           8
        .value_kind:     global_buffer
    .group_segment_fixed_size: 12288
    .kernarg_segment_align: 8
    .kernarg_segment_size: 40
    .language:       OpenCL C
    .language_version:
      - 2
      - 0
    .max_flat_workgroup_size: 256
    .name:           _Z11k_ret_naivePKtS0_S0_PKfPf
    .private_segment_fixed_size: 0
    .sgpr_count:     22
    .sgpr_spill_count: 0
    .symbol:         _Z11k_ret_naivePKtS0_S0_PKfPf.kd
    .uniform_work_group_size: 1
    .uses_dynamic_stack: false
    .vgpr_count:     234
    .vgpr_spill_count: 0
    .wavefront_size: 64
; DI float bflo(unsigned w) { return __uint_as_float(w << 16); }
; DI float bfhi(unsigned w) { return __uint_as_float(w & 0xffff0000u); }
; DI unsigned pk2(float lo, float hi) { unsigned r; asm("v_cvt_pk_bf16_f32 %0, %1, %2" : "=v"(r) : "v"(lo), "v"(hi)); return r; }
; #define LAS __attribute__((address_space(3)))
; __global__ void __launch_bounds__(256) k_ret_norm(const float* __restrict__ Oraw, const float* __restrict__ gain, const bf16_t* __restrict__ RG, bf16_t* __restrict__ MIXIN) {
;     const int lane = threadIdx.x & 63, w = blockIdx.x * 4 + (threadIdx.x >> 6);
;     const int bh = w >> 12, s = w & 4095, b = bh >> 3, h = bh & 7;
;     const f32x2 v = *(const f32x2*)(Oraw + ((size_t)bh * S + s) * 128 + 2 * lane);
;     const float mu = wave_sum(v.x + v.y) * (1.f / 128.f);
;     const float d0 = v.x - mu, d1 = v.y - mu;
;     const float var = wave_sum(d0 * d0 + d1 * d1) * (1.f / 128.f);
;     const float rs = rsqrtf(var + NORM_EPS);
;     const size_t tok = (size_t)b * S + s;
;     const unsigned g = *(const unsigned*)(RG + tok * 1024 + h * 128 + 2 * lane);
;     *(unsigned*)(MIXIN + tok * D + 1024 + h * 128 + 2 * lane) = pk2(d0 * rs * gain[h * 128 + 2 * lane] * bflo(g), d1 * rs * gain[h * 128 + 2 * lane + 1] * bfhi(g));
; }
; __global__ void __launch_bounds__(NTHR, 2) mega(Args a) {
;     extern __shared__ __attribute__((aligned(16))) unsigned char lds[];
;     Frame F;
;     F.lds = lds; F.ldsl = (LAS unsigned char*)lds; F.ws = a.ws; F.in = a.in; F.out = a.out;
;     F.wg = blockIdx.x; F.nwg = gridDim.x;
;     F.wave = __builtin_amdgcn_readfirstlane(threadIdx.x >> 6);
  - .agpr_count:     0
    .args:
      - .actual_access:  read_only
        .address_space:  global
        .offset:         0
        .size:           8
        .value_kind:     global_buffer
      - .actual_access:  read_only
        .address_space:  global
        .offset:         8
        .size:           8
        .value_kind:     global_buffer
      - .actual_access:  read_only
        .address_space:  global
        .offset:         16
        .size:           8
        .value_kind:     global_buffer
      - .actual_access:  write_only
        .address_space:  global
        .offset:         24
        .size:           8
        .value_kind:     global_buffer
    .group_segment_fixed_size: 0
    .kernarg_segment_align: 8
    .kernarg_segment_size: 32
    .language:       OpenCL C
    .language_version:
      - 2
      - 0
    .max_flat_workgroup_size: 256
    .name:           _Z10k_ret_normPKfS0_PKtPt
    .private_segment_fixed_size: 0
    .sgpr_count:     20
    .sgpr_spill_count: 0
    .symbol:         _Z10k_ret_normPKfS0_PKtPt.kd
    .uniform_work_group_size: 1
    .uses_dynamic_stack: false
    .vgpr_count:     12
    .vgpr_spill_count: 0
    .wavefront_size: 64
  - .agpr_count:     0
    .args:
      - .offset:         0
        .size:           200
        .value_kind:     by_value
      - .offset:         200
        .size:           4
        .value_kind:     hidden_block_count_x
      - .offset:         204
        .size:           4
        .value_kind:     hidden_block_count_y
      - .offset:         208
        .size:           4
        .value_kind:     hidden_block_count_z
      - .offset:         212
        .size:           2
        .value_kind:     hidden_group_size_x
      - .offset:         214
        .size:           2
        .value_kind:     hidden_group_size_y
      - .offset:         216
        .size:           2
        .value_kind:     hidden_group_size_z
      - .offset:         218
        .size:           2
        .value_kind:     hidden_remainder_x
      - .offset:         220
        .size:           2
        .value_kind:     hidden_remainder_y
      - .offset:         222
        .size:           2
        .value_kind:     hidden_remainder_z
      - .offset:         240
        .size:           8
        .value_kind:     hidden_global_offset_x
      - .offset:         248
        .size:           8
        .value_kind:     hidden_global_offset_y
      - .offset:         256
        .size:           8
        .value_kind:     hidden_global_offset_z
      - .offset:         264
        .size:           2
        .value_kind:     hidden_grid_dims
      - .offset:         320
        .size:           4
        .value_kind:     hidden_dynamic_lds_size
    .group_segment_fixed_size: 0
    .kernarg_segment_align: 8
    .kernarg_segment_size: 456
    .language:       OpenCL C
    .language_version:
      - 2
      - 0
    .max_flat_workgroup_size: 512
    .name:           _Z4mega4Args
    .private_segment_fixed_size: 0
    .sgpr_count:     108
    .sgpr_spill_count: 0
    .symbol:         _Z4mega4Args.kd
    .uniform_work_group_size: 1
    .uses_dynamic_stack: false
    .vgpr_count:     256
    .vgpr_spill_count: 0
    .wavefront_size: 64
